# diff-attn main loops duplicated: a check-free copy for the fixed-reference mode, the tested copy for redone units
# speedup vs baseline: 1.0181x; 1.0181x over previous
.LBB0_1211:
	s_and_b32 s37, s95, 0xffffffc0
	v_lshlrev_b32_e32 v6, 2, v5
	v_lshlrev_b32_e32 v3, 6, v4
	v_and_b32_e32 v6, 48, v6
	s_cmp_lg_u32 0, -1
	v_bitop3_b32 v194, v6, v3, v2 bitop3:0xde
	s_cselect_b32 s38, 0, 0
	v_lshlrev_b32_e32 v2, 3, v5
	v_and_b32_e32 v193, 63, v5
	v_add_u32_e32 v183, s38, v194
	s_addk_i32 s38, 0x4000
	v_and_b32_e32 v2, 32, v2
	s_lshl_b32 s37, s37, 2
	v_add_u32_e32 v188, s38, v194
	v_sub_u32_e32 v195, 16, v2
	v_lshrrev_b32_e32 v2, 5, v193
	s_add_i32 s78, s37, 0
	v_add_u32_e32 v190, v183, v195
	s_mov_b64 s[38:39], -1
	s_and_b64 vcc, exec, s[6:7]
	v_add_u32_e32 v189, v188, v195
	v_cmp_gt_u32_e64 s[6:7], 32, v193
	v_lshlrev_b32_e32 v186, 4, v2
	v_lshl_add_u32 v187, v4, 2, s78
	v_and_b32_e32 v248, 31, v193
	v_mov_b32_e32 v249, 0x38383838
	v_cmp_eq_u32_e64 s[100:101], 0, v248
	v_lshrrev_b32_e32 v250, 4, v193
	s_nop 0
	v_cndmask_b32_e64 v146, 0, v249, s[100:101]
	v_cmp_eq_u32_e64 s[100:101], 17, v248
	v_and_b32_e32 v248, 15, v193
	v_lshlrev_b32_e32 v248, 6, v248
	v_cndmask_b32_e64 v146, v146, v249, s[100:101]
	v_lshl_add_u32 v250, v250, 4, v248
	v_add_u32_e32 v250, s78, v250
	v_mov_b32_e32 v147, v146
	v_mov_b32_e32 v148, v146
	v_mov_b32_e32 v149, v146
	v_mov_b32_e32 v150, v146
	v_mov_b32_e32 v151, v146
	v_mov_b32_e32 v152, v146
	v_mov_b32_e32 v153, v146
	s_cbranch_vccz .LBB0_1264
	ds_read_b128 v[18:21], v183 offset:0
	ds_read_b128 v[22:25], v190 offset:0
	ds_read_b128 v[34:37], v183 offset:0x800
	ds_read_b128 v[38:41], v190 offset:0x800
	s_waitcnt lgkmcnt(0)
	s_waitcnt vmcnt(0)
	v_mfma_f32_32x32x64_f8f6f4 v[18:33], v[18:25], v[154:161], 0
	s_mov_b32 s37, s36
	s_mov_b32 s38, s36
	s_mov_b32 s39, s36
	s_mov_b32 s40, s36
	s_mov_b32 s41, s36
	s_mov_b32 s42, s36
	s_mov_b32 s43, s36
	s_mov_b32 s44, s36
	s_mov_b32 s45, s36
	s_mov_b32 s46, s36
	s_mov_b32 s47, s36
	s_mov_b32 s48, s36
	s_mov_b32 s49, s36
	s_mov_b32 s50, s36
	s_mov_b32 s51, s36
	v_mov_b64_e32 v[2:3], s[36:37]
	v_mov_b64_e32 v[4:5], s[38:39]
	v_mov_b64_e32 v[6:7], s[40:41]
	v_mov_b64_e32 v[8:9], s[42:43]
	v_mov_b64_e32 v[10:11], s[44:45]
	v_mov_b64_e32 v[12:13], s[46:47]
	v_mov_b64_e32 v[14:15], s[48:49]
	v_mov_b64_e32 v[16:17], s[50:51]
	v_max_f32_e32 v42, v19, v19
	v_max_f32_e32 v43, v18, v18
	v_max_f32_e32 v42, v43, v42
	v_max3_f32 v42, v42, v20, v21
	v_max3_f32 v42, v42, v22, v23
	v_max3_f32 v42, v42, v24, v25
	v_max3_f32 v42, v42, v26, v27
	v_max3_f32 v42, v42, v28, v29
	v_max3_f32 v50, v42, v30, v31
	v_mfma_f32_32x32x64_f8f6f4 v[34:49], v[34:41], v[154:161], 0
	v_max3_f32 v50, v50, v32, v33
	s_cmp_lg_u32 0, -1
	s_cselect_b32 s37, 0, 0
	v_mov_b32_e32 v130, v181
	v_mov_b32_e32 v131, v181
	s_add_i32 s38, s37, 0x1000
	s_waitcnt vmcnt(0) lgkmcnt(0)
	s_barrier
	v_add_u32_e32 v207, s38, v194
	v_add_u32_e32 v209, v207, v195
	s_nop 11
	v_max3_f32 v50, v50, v34, v35
	v_max3_f32 v50, v50, v36, v37
	v_max3_f32 v50, v50, v38, v39
	v_max3_f32 v50, v50, v40, v41
	v_max3_f32 v50, v50, v42, v43
	v_max3_f32 v50, v50, v44, v45
	v_max3_f32 v50, v50, v46, v47
	v_max3_f32 v50, v50, v48, v49
	v_mov_b32_e32 v51, v50
	s_nop 1
	v_permlane32_swap_b32_e32 v50, v51
	v_max_f32_e32 v51, v51, v51
	v_max_f32_e32 v50, v50, v50
	v_max_f32_e32 v50, v50, v51
	s_cmp_eq_u32 s98, 0
	s_cselect_b32 s100, 0x40000000, 0xc0600000
	v_add_f32_e32 v198, s100, v50
	v_sub_f32_e32 v18, v18, v198
	v_sub_f32_e32 v19, v19, v198
	v_sub_f32_e32 v22, v22, v198
	v_sub_f32_e32 v23, v23, v198
	v_exp_f32_e32 v50, v18
	v_exp_f32_e32 v51, v19
	v_exp_f32_e32 v54, v22
	v_exp_f32_e32 v55, v23
	v_xor_b32_e32 v82, 0x80000000, v198
	v_sub_f32_e32 v20, v20, v198
	v_sub_f32_e32 v21, v21, v198
	v_sub_f32_e32 v24, v24, v198
	v_sub_f32_e32 v25, v25, v198
	v_mov_b32_e32 v83, v82
	v_mov_b32_e32 v84, v82
	v_mov_b32_e32 v85, v82
	v_mov_b32_e32 v86, v82
	v_mov_b32_e32 v87, v82
	v_mov_b32_e32 v88, v82
	v_mov_b32_e32 v89, v82
	v_mov_b32_e32 v90, v82
	v_mov_b32_e32 v91, v82
	v_mov_b32_e32 v92, v82
	v_mov_b32_e32 v93, v82
	v_mov_b32_e32 v94, v82
	v_mov_b32_e32 v95, v82
	v_mov_b32_e32 v96, v82
	v_mov_b32_e32 v97, v82
	v_exp_f32_e32 v52, v20
	v_exp_f32_e32 v53, v21
	v_exp_f32_e32 v56, v24
	v_exp_f32_e32 v57, v25
	v_cvt_pk_fp8_f32 v130, v50, v51
	v_cvt_pk_fp8_f32 v131, v54, v55
	ds_read_b128 v[18:21], v207 offset:0
	v_sub_f32_e32 v26, v26, v198
	v_sub_f32_e32 v27, v27, v198
	v_sub_f32_e32 v28, v28, v198
	v_sub_f32_e32 v29, v29, v198
	ds_read_b128 v[22:25], v209 offset:0
	v_sub_f32_e32 v34, v34, v198
	v_sub_f32_e32 v35, v35, v198
	v_sub_f32_e32 v36, v36, v198
	v_sub_f32_e32 v37, v37, v198
	v_sub_f32_e32 v38, v38, v198
	v_sub_f32_e32 v39, v39, v198
	v_sub_f32_e32 v40, v40, v198
	v_sub_f32_e32 v41, v41, v198
	v_sub_f32_e32 v42, v42, v198
	v_sub_f32_e32 v43, v43, v198
	v_sub_f32_e32 v44, v44, v198
	v_sub_f32_e32 v45, v45, v198
	v_sub_f32_e32 v30, v30, v198
	v_sub_f32_e32 v46, v46, v198
	v_sub_f32_e32 v31, v31, v198
	v_sub_f32_e32 v47, v47, v198
	v_sub_f32_e32 v32, v32, v198
	v_sub_f32_e32 v48, v48, v198
	v_sub_f32_e32 v33, v33, v198
	v_sub_f32_e32 v49, v49, v198
	v_exp_f32_e32 v58, v26
	v_exp_f32_e32 v59, v27
	v_exp_f32_e32 v60, v28
	v_exp_f32_e32 v61, v29
	ds_read_b128 v[26:29], v207 offset:0x800
	v_exp_f32_e32 v34, v34
	v_exp_f32_e32 v35, v35
	v_exp_f32_e32 v36, v36
	v_exp_f32_e32 v37, v37
	v_exp_f32_e32 v38, v38
	v_exp_f32_e32 v39, v39
	v_exp_f32_e32 v40, v40
	v_exp_f32_e32 v41, v41
	v_exp_f32_e32 v42, v42
	v_exp_f32_e32 v43, v43
	v_exp_f32_e32 v44, v44
	v_exp_f32_e32 v45, v45
	v_exp_f32_e32 v62, v30
	v_exp_f32_e32 v46, v46
	v_exp_f32_e32 v63, v31
	v_exp_f32_e32 v47, v47
	v_exp_f32_e32 v64, v32
	v_exp_f32_e32 v48, v48
	v_exp_f32_e32 v65, v33
	v_exp_f32_e32 v49, v49
	ds_read_b128 v[30:33], v209 offset:0x800
	v_cvt_pk_fp8_f32 v130, v52, v53 op_sel:[0,0,1]
	v_cvt_pk_fp8_f32 v131, v56, v57 op_sel:[0,0,1]
	s_waitcnt lgkmcnt(2)
	v_mfma_f32_32x32x64_f8f6f4 v[98:113], v[18:25], v[154:161], v[82:97]
	v_mov_b32_e32 v132, v181
	v_mov_b32_e32 v133, v181
	v_cvt_pk_fp8_f32 v132, v58, v59
	v_cvt_pk_fp8_f32 v133, v62, v63
	ds_read_b128 v[170:173], v188 offset:0
	ds_read_b128 v[174:177], v189 offset:0
	v_cvt_pk_fp8_f32 v132, v60, v61 op_sel:[0,0,1]
	v_cvt_pk_fp8_f32 v133, v64, v65 op_sel:[0,0,1]
	s_waitcnt lgkmcnt(2)
	v_mov_b64_e32 v[128:129], v[96:97]
	v_mov_b64_e32 v[126:127], v[94:95]
	v_mov_b64_e32 v[124:125], v[92:93]
	v_mov_b64_e32 v[122:123], v[90:91]
	v_mov_b64_e32 v[120:121], v[88:89]
	v_mov_b64_e32 v[118:119], v[86:87]
	v_mov_b64_e32 v[116:117], v[84:85]
	v_mov_b64_e32 v[114:115], v[82:83]
	v_mov_b32_e32 v134, v181
	v_mov_b32_e32 v135, v181
	v_mfma_f32_32x32x64_f8f6f4 v[114:129], v[26:33], v[154:161], v[114:129]
	v_mov_b32_e32 v136, v181
	v_mov_b32_e32 v137, v181
	v_cvt_pk_fp8_f32 v134, v34, v35
	v_cvt_pk_fp8_f32 v135, v38, v39
	v_cvt_pk_fp8_f32 v136, v42, v43
	v_cvt_pk_fp8_f32 v137, v46, v47
	v_cvt_pk_fp8_f32 v134, v36, v37 op_sel:[0,0,1]
	v_cvt_pk_fp8_f32 v135, v40, v41 op_sel:[0,0,1]
	v_cvt_pk_fp8_f32 v136, v44, v45 op_sel:[0,0,1]
	v_cvt_pk_fp8_f32 v137, v48, v49 op_sel:[0,0,1]
	s_nop 0
	ds_read_b128 v[138:141], v188 offset:0x800
	ds_read_b128 v[142:145], v189 offset:0x800
	s_nop 0
	v_mfma_f32_16x16x128_f8f6f4 v[18:21], v[130:137], v[146:153], 0
	s_add_i32 s38, s37, 0x2000
	v_add_u32_e32 v205, s38, v194
	s_add_i32 s38, s37, 0x6000
	v_add_u32_e32 v203, s38, v194
	s_add_i32 s38, s37, 0x3000
	s_waitcnt vmcnt(0) lgkmcnt(0)
	s_barrier
	v_add_u32_e32 v201, s38, v194
	s_add_i32 s38, s37, 0x8000
	s_add_i32 s37, s37, 0xa000
	v_add_u32_e32 v199, s38, v194
	v_add_u32_e32 v196, s37, v194
	v_mov_b64_e32 v[48:49], v[16:17]
	v_mov_b64_e32 v[64:65], v[16:17]
	v_mov_b64_e32 v[80:81], v[16:17]
	v_add_u32_e32 v206, v205, v195
	v_add_u32_e32 v204, v203, v195
	v_add_u32_e32 v202, v201, v195
	v_add_u32_e32 v200, v199, v195
	v_add_u32_e32 v197, v196, v195
	s_mov_b32 s37, -2
	v_mov_b64_e32 v[46:47], v[14:15]
	v_mov_b64_e32 v[44:45], v[12:13]
	v_mov_b64_e32 v[42:43], v[10:11]
	v_mov_b64_e32 v[40:41], v[8:9]
	v_mov_b64_e32 v[38:39], v[6:7]
	v_mov_b64_e32 v[36:37], v[4:5]
	v_mov_b64_e32 v[34:35], v[2:3]
	v_mov_b64_e32 v[62:63], v[14:15]
	v_mov_b64_e32 v[60:61], v[12:13]
	v_mov_b64_e32 v[58:59], v[10:11]
	v_mov_b64_e32 v[56:57], v[8:9]
	v_mov_b64_e32 v[54:55], v[6:7]
	v_mov_b64_e32 v[52:53], v[4:5]
	v_mov_b64_e32 v[50:51], v[2:3]
	v_mov_b64_e32 v[78:79], v[14:15]
	v_mov_b64_e32 v[76:77], v[12:13]
	v_mov_b64_e32 v[74:75], v[10:11]
	v_mov_b64_e32 v[72:73], v[8:9]
	v_mov_b64_e32 v[70:71], v[6:7]
	v_mov_b64_e32 v[68:69], v[4:5]
	v_mov_b64_e32 v[66:67], v[2:3]
	s_cmp_lg_u32 s98, 0
	s_cbranch_scc1 .LBB0_1215
	s_branch .Lf_1215

.LBB0_1239:
	s_waitcnt lgkmcnt(2)
	v_mfma_f32_32x32x64_f8f6f4 v[34:49], v[130:137], v[162:169], v[34:49]
	ds_read_b128 v[162:165], v196 offset:0x1800
	ds_read_b128 v[166:169], v197 offset:0x1800
	v_exp_f32_e32 v98, v98
	v_exp_f32_e32 v99, v99
	v_exp_f32_e32 v100, v100
	v_exp_f32_e32 v101, v101
	v_exp_f32_e32 v102, v102
	v_exp_f32_e32 v103, v103
	v_exp_f32_e32 v104, v104
	v_exp_f32_e32 v105, v105
	v_exp_f32_e32 v106, v106
	v_exp_f32_e32 v107, v107
	v_exp_f32_e32 v108, v108
	s_waitcnt lgkmcnt(2)
	v_mfma_f32_32x32x64_f8f6f4 v[50:65], v[130:137], v[138:145], v[50:65]
	v_exp_f32_e32 v109, v109
	v_exp_f32_e32 v110, v110
	v_exp_f32_e32 v111, v111
	v_exp_f32_e32 v112, v112
	v_exp_f32_e32 v113, v113
	v_exp_f32_e32 v114, v114
	v_exp_f32_e32 v115, v115
	v_exp_f32_e32 v116, v116
	v_exp_f32_e32 v117, v117
	v_exp_f32_e32 v118, v118
	v_exp_f32_e32 v119, v119
	s_waitcnt lgkmcnt(0)
	v_mfma_f32_32x32x64_f8f6f4 v[66:81], v[130:137], v[162:169], v[66:81]
	v_exp_f32_e32 v120, v120
	v_exp_f32_e32 v121, v121
	v_exp_f32_e32 v122, v122
	v_exp_f32_e32 v123, v123
	v_exp_f32_e32 v124, v124
	v_exp_f32_e32 v125, v125
	v_exp_f32_e32 v126, v126
	v_exp_f32_e32 v127, v127
	v_exp_f32_e32 v128, v128
	v_exp_f32_e32 v129, v129
	s_andn2_b64 vcc, exec, s[38:39]
	s_cbranch_vccnz .LBB0_1214
	s_and_saveexec_b64 s[38:39], s[6:7]
	s_cbranch_execz .LBB0_1213
	ds_write_b32 v187, v170 offset:49152
	s_branch .LBB0_1213
.Lf_1214:
	v_cvt_pk_fp8_f32 v130, v98, v99
	v_cvt_pk_fp8_f32 v131, v102, v103
	ds_read_b128 v[138:141], v207 offset:0
	ds_read_b128 v[142:145], v209 offset:0
	ds_read_b128 v[162:165], v207 offset:0x800
	ds_read_b128 v[166:169], v209 offset:0x800
	v_cvt_pk_fp8_f32 v130, v100, v101 op_sel:[0,0,1]
	v_cvt_pk_fp8_f32 v131, v104, v105 op_sel:[0,0,1]
	s_waitcnt lgkmcnt(2)
	v_cvt_pk_fp8_f32 v132, v106, v107
	v_cvt_pk_fp8_f32 v133, v110, v111
	ds_read_b128 v[170:173], v188 offset:0
	ds_read_b128 v[174:177], v189 offset:0
	v_cvt_pk_fp8_f32 v132, v108, v109 op_sel:[0,0,1]
	v_cvt_pk_fp8_f32 v133, v112, v113 op_sel:[0,0,1]
	v_mfma_f32_32x32x64_f8f6f4 v[98:113], v[138:145], v[154:161], v[82:97]
	s_waitcnt lgkmcnt(2)
	v_cvt_pk_fp8_f32 v134, v114, v115
	v_cvt_pk_fp8_f32 v135, v118, v119
	v_cvt_pk_fp8_f32 v136, v122, v123
	v_cvt_pk_fp8_f32 v137, v126, v127
	v_cvt_pk_fp8_f32 v134, v116, v117 op_sel:[0,0,1]
	v_cvt_pk_fp8_f32 v135, v120, v121 op_sel:[0,0,1]
	v_cvt_pk_fp8_f32 v136, v124, v125 op_sel:[0,0,1]
	v_cvt_pk_fp8_f32 v137, v128, v129 op_sel:[0,0,1]
	v_mfma_f32_32x32x64_f8f6f4 v[114:129], v[162:169], v[154:161], v[82:97]
	ds_read_b128 v[138:141], v188 offset:0x800
	ds_read_b128 v[142:145], v189 offset:0x800
	s_nop 0
	v_mfma_f32_16x16x128_f8f6f4 v[18:21], v[130:137], v[146:153], v[18:21]
	s_waitcnt vmcnt(0) lgkmcnt(0)
	s_barrier
	s_add_i32 s37, s37, 4
	s_cmpk_lt_u32 s37, 0xfb
	s_cbranch_scc0 .LBB0_1242
.Lf_1215:
	s_waitcnt lgkmcnt(2)
	v_mfma_f32_32x32x64_f8f6f4 v[2:17], v[130:137], v[170:177], v[2:17]
	ds_read_b128 v[162:165], v188 offset:0x1000
	ds_read_b128 v[166:169], v189 offset:0x1000
.Lf_1218:
	s_waitcnt lgkmcnt(2)
	v_mfma_f32_32x32x64_f8f6f4 v[34:49], v[130:137], v[138:145], v[34:49]
	ds_read_b128 v[138:141], v188 offset:0x1800
	ds_read_b128 v[142:145], v189 offset:0x1800
	v_exp_f32_e32 v98, v98
	v_exp_f32_e32 v99, v99
	v_exp_f32_e32 v100, v100
	v_exp_f32_e32 v101, v101
	v_exp_f32_e32 v102, v102
	v_exp_f32_e32 v103, v103
	v_exp_f32_e32 v104, v104
	v_exp_f32_e32 v105, v105
	v_exp_f32_e32 v106, v106
	v_exp_f32_e32 v107, v107
	v_exp_f32_e32 v108, v108
	s_waitcnt lgkmcnt(2)
	v_mfma_f32_32x32x64_f8f6f4 v[50:65], v[130:137], v[162:169], v[50:65]
	v_exp_f32_e32 v109, v109
	v_exp_f32_e32 v110, v110
	v_exp_f32_e32 v111, v111
	v_exp_f32_e32 v112, v112
	v_exp_f32_e32 v113, v113
	v_exp_f32_e32 v114, v114
	v_exp_f32_e32 v115, v115
	v_exp_f32_e32 v116, v116
	v_exp_f32_e32 v117, v117
	v_exp_f32_e32 v118, v118
	v_exp_f32_e32 v119, v119
	s_waitcnt lgkmcnt(0)
	v_mfma_f32_32x32x64_f8f6f4 v[66:81], v[130:137], v[138:145], v[66:81]
	v_exp_f32_e32 v120, v120
	v_exp_f32_e32 v121, v121
	v_exp_f32_e32 v122, v122
	v_exp_f32_e32 v123, v123
	v_exp_f32_e32 v124, v124
	v_exp_f32_e32 v125, v125
	v_exp_f32_e32 v126, v126
	v_exp_f32_e32 v127, v127
	v_exp_f32_e32 v128, v128
	v_exp_f32_e32 v129, v129
.Lf_1222:
	v_cvt_pk_fp8_f32 v130, v98, v99
	v_cvt_pk_fp8_f32 v131, v102, v103
	ds_read_b128 v[138:141], v205 offset:0
	ds_read_b128 v[142:145], v206 offset:0
	ds_read_b128 v[170:173], v205 offset:0x800
	ds_read_b128 v[174:177], v206 offset:0x800
	v_cvt_pk_fp8_f32 v130, v100, v101 op_sel:[0,0,1]
	v_cvt_pk_fp8_f32 v131, v104, v105 op_sel:[0,0,1]
	s_waitcnt lgkmcnt(2)
	v_cvt_pk_fp8_f32 v132, v106, v107
	v_cvt_pk_fp8_f32 v133, v110, v111
	ds_read_b128 v[210:213], v203 offset:0
	ds_read_b128 v[214:217], v204 offset:0
	v_cvt_pk_fp8_f32 v132, v108, v109 op_sel:[0,0,1]
	v_cvt_pk_fp8_f32 v133, v112, v113 op_sel:[0,0,1]
	v_mfma_f32_32x32x64_f8f6f4 v[98:113], v[138:145], v[154:161], v[82:97]
	s_waitcnt lgkmcnt(2)
	v_cvt_pk_fp8_f32 v134, v114, v115
	v_cvt_pk_fp8_f32 v135, v118, v119
	v_cvt_pk_fp8_f32 v136, v122, v123
	v_cvt_pk_fp8_f32 v137, v126, v127
	v_cvt_pk_fp8_f32 v134, v116, v117 op_sel:[0,0,1]
	v_cvt_pk_fp8_f32 v135, v120, v121 op_sel:[0,0,1]
	v_cvt_pk_fp8_f32 v136, v124, v125 op_sel:[0,0,1]
	v_cvt_pk_fp8_f32 v137, v128, v129 op_sel:[0,0,1]
	v_mfma_f32_32x32x64_f8f6f4 v[114:129], v[170:177], v[154:161], v[82:97]
	ds_read_b128 v[162:165], v203 offset:0x800
	ds_read_b128 v[166:169], v204 offset:0x800
	s_nop 0
	v_mfma_f32_16x16x128_f8f6f4 v[18:21], v[130:137], v[146:153], v[18:21]
	s_waitcnt vmcnt(0) lgkmcnt(0)
	s_barrier
	s_waitcnt lgkmcnt(2)
	v_mfma_f32_32x32x64_f8f6f4 v[2:17], v[130:137], v[210:217], v[2:17]
	ds_read_b128 v[138:141], v203 offset:0x1000
	ds_read_b128 v[142:145], v204 offset:0x1000
.Lf_1225:
	s_waitcnt lgkmcnt(2)
	v_mfma_f32_32x32x64_f8f6f4 v[34:49], v[130:137], v[162:169], v[34:49]
	ds_read_b128 v[162:165], v203 offset:0x1800
	ds_read_b128 v[166:169], v204 offset:0x1800
	v_exp_f32_e32 v98, v98
	v_exp_f32_e32 v99, v99
	v_exp_f32_e32 v100, v100
	v_exp_f32_e32 v101, v101
	v_exp_f32_e32 v102, v102
	v_exp_f32_e32 v103, v103
	v_exp_f32_e32 v104, v104
	v_exp_f32_e32 v105, v105
	v_exp_f32_e32 v106, v106
	v_exp_f32_e32 v107, v107
	v_exp_f32_e32 v108, v108
	s_waitcnt lgkmcnt(2)
	v_mfma_f32_32x32x64_f8f6f4 v[50:65], v[130:137], v[138:145], v[50:65]
	v_exp_f32_e32 v109, v109
	v_exp_f32_e32 v110, v110
	v_exp_f32_e32 v111, v111
	v_exp_f32_e32 v112, v112
	v_exp_f32_e32 v113, v113
	v_exp_f32_e32 v114, v114
	v_exp_f32_e32 v115, v115
	v_exp_f32_e32 v116, v116
	v_exp_f32_e32 v117, v117
	v_exp_f32_e32 v118, v118
	v_exp_f32_e32 v119, v119
	s_waitcnt lgkmcnt(0)
	v_mfma_f32_32x32x64_f8f6f4 v[66:81], v[130:137], v[162:169], v[66:81]
	v_exp_f32_e32 v120, v120
	v_exp_f32_e32 v121, v121
	v_exp_f32_e32 v122, v122
	v_exp_f32_e32 v123, v123
	v_exp_f32_e32 v124, v124
	v_exp_f32_e32 v125, v125
	v_exp_f32_e32 v126, v126
	v_exp_f32_e32 v127, v127
	v_exp_f32_e32 v128, v128
	v_exp_f32_e32 v129, v129
.Lf_1229:
	v_cvt_pk_fp8_f32 v130, v98, v99
	v_cvt_pk_fp8_f32 v131, v102, v103
	ds_read_b128 v[138:141], v201 offset:0
	ds_read_b128 v[142:145], v202 offset:0
	ds_read_b128 v[170:173], v201 offset:0x800
	ds_read_b128 v[174:177], v202 offset:0x800
	v_cvt_pk_fp8_f32 v130, v100, v101 op_sel:[0,0,1]
	v_cvt_pk_fp8_f32 v131, v104, v105 op_sel:[0,0,1]
	s_waitcnt lgkmcnt(2)
	v_cvt_pk_fp8_f32 v132, v106, v107
	v_cvt_pk_fp8_f32 v133, v110, v111
	ds_read_b128 v[210:213], v199 offset:0
	ds_read_b128 v[214:217], v200 offset:0
	v_cvt_pk_fp8_f32 v132, v108, v109 op_sel:[0,0,1]
	v_cvt_pk_fp8_f32 v133, v112, v113 op_sel:[0,0,1]
	v_mfma_f32_32x32x64_f8f6f4 v[98:113], v[138:145], v[154:161], v[82:97]
	s_waitcnt lgkmcnt(2)
	v_cvt_pk_fp8_f32 v134, v114, v115
	v_cvt_pk_fp8_f32 v135, v118, v119
	v_cvt_pk_fp8_f32 v136, v122, v123
	v_cvt_pk_fp8_f32 v137, v126, v127
	v_cvt_pk_fp8_f32 v134, v116, v117 op_sel:[0,0,1]
	v_cvt_pk_fp8_f32 v135, v120, v121 op_sel:[0,0,1]
	v_cvt_pk_fp8_f32 v136, v124, v125 op_sel:[0,0,1]
	v_cvt_pk_fp8_f32 v137, v128, v129 op_sel:[0,0,1]
	v_mfma_f32_32x32x64_f8f6f4 v[114:129], v[170:177], v[154:161], v[82:97]
	ds_read_b128 v[162:165], v199 offset:0x800
	ds_read_b128 v[166:169], v200 offset:0x800
	s_nop 0
	v_mfma_f32_16x16x128_f8f6f4 v[18:21], v[130:137], v[146:153], v[18:21]
	s_waitcnt vmcnt(0) lgkmcnt(0)
	s_barrier
	s_waitcnt lgkmcnt(2)
	v_mfma_f32_32x32x64_f8f6f4 v[2:17], v[130:137], v[210:217], v[2:17]
	ds_read_b128 v[138:141], v199 offset:0x1000
	ds_read_b128 v[142:145], v200 offset:0x1000
.Lf_1232:
	s_waitcnt lgkmcnt(2)
	v_mfma_f32_32x32x64_f8f6f4 v[34:49], v[130:137], v[162:169], v[34:49]
	ds_read_b128 v[162:165], v199 offset:0x1800
	ds_read_b128 v[166:169], v200 offset:0x1800
	v_exp_f32_e32 v98, v98
	v_exp_f32_e32 v99, v99
	v_exp_f32_e32 v100, v100
	v_exp_f32_e32 v101, v101
	v_exp_f32_e32 v102, v102
	v_exp_f32_e32 v103, v103
	v_exp_f32_e32 v104, v104
	v_exp_f32_e32 v105, v105
	v_exp_f32_e32 v106, v106
	v_exp_f32_e32 v107, v107
	v_exp_f32_e32 v108, v108
	s_waitcnt lgkmcnt(2)
	v_mfma_f32_32x32x64_f8f6f4 v[50:65], v[130:137], v[138:145], v[50:65]
	v_exp_f32_e32 v109, v109
	v_exp_f32_e32 v110, v110
	v_exp_f32_e32 v111, v111
	v_exp_f32_e32 v112, v112
	v_exp_f32_e32 v113, v113
	v_exp_f32_e32 v114, v114
	v_exp_f32_e32 v115, v115
	v_exp_f32_e32 v116, v116
	v_exp_f32_e32 v117, v117
	v_exp_f32_e32 v118, v118
	v_exp_f32_e32 v119, v119
	s_waitcnt lgkmcnt(0)
	v_mfma_f32_32x32x64_f8f6f4 v[66:81], v[130:137], v[162:169], v[66:81]
	v_exp_f32_e32 v120, v120
	v_exp_f32_e32 v121, v121
	v_exp_f32_e32 v122, v122
	v_exp_f32_e32 v123, v123
	v_exp_f32_e32 v124, v124
	v_exp_f32_e32 v125, v125
	v_exp_f32_e32 v126, v126
	v_exp_f32_e32 v127, v127
	v_exp_f32_e32 v128, v128
	v_exp_f32_e32 v129, v129
.Lf_1236:
	v_cvt_pk_fp8_f32 v130, v98, v99
	v_cvt_pk_fp8_f32 v131, v102, v103
	ds_read_b128 v[138:141], v183 offset:0
	ds_read_b128 v[142:145], v190 offset:0
	ds_read_b128 v[170:173], v183 offset:0x800
	ds_read_b128 v[174:177], v190 offset:0x800
	v_cvt_pk_fp8_f32 v130, v100, v101 op_sel:[0,0,1]
	v_cvt_pk_fp8_f32 v131, v104, v105 op_sel:[0,0,1]
	s_waitcnt lgkmcnt(2)
	v_cvt_pk_fp8_f32 v132, v106, v107
	v_cvt_pk_fp8_f32 v133, v110, v111
	ds_read_b128 v[210:213], v196 offset:0
	ds_read_b128 v[214:217], v197 offset:0
	v_cvt_pk_fp8_f32 v132, v108, v109 op_sel:[0,0,1]
	v_cvt_pk_fp8_f32 v133, v112, v113 op_sel:[0,0,1]
	v_mfma_f32_32x32x64_f8f6f4 v[98:113], v[138:145], v[154:161], v[82:97]
	s_waitcnt lgkmcnt(2)
	v_cvt_pk_fp8_f32 v134, v114, v115
	v_cvt_pk_fp8_f32 v135, v118, v119
	v_cvt_pk_fp8_f32 v136, v122, v123
	v_cvt_pk_fp8_f32 v137, v126, v127
	v_cvt_pk_fp8_f32 v134, v116, v117 op_sel:[0,0,1]
	v_cvt_pk_fp8_f32 v135, v120, v121 op_sel:[0,0,1]
	v_cvt_pk_fp8_f32 v136, v124, v125 op_sel:[0,0,1]
	v_cvt_pk_fp8_f32 v137, v128, v129 op_sel:[0,0,1]
	v_mfma_f32_32x32x64_f8f6f4 v[114:129], v[170:177], v[154:161], v[82:97]
	ds_read_b128 v[162:165], v196 offset:0x800
	ds_read_b128 v[166:169], v197 offset:0x800
	s_nop 0
	v_mfma_f32_16x16x128_f8f6f4 v[18:21], v[130:137], v[146:153], v[18:21]
	s_waitcnt vmcnt(0) lgkmcnt(0)
	s_barrier
	s_waitcnt lgkmcnt(2)
	v_mfma_f32_32x32x64_f8f6f4 v[2:17], v[130:137], v[210:217], v[2:17]
	ds_read_b128 v[138:141], v196 offset:0x1000
	ds_read_b128 v[142:145], v197 offset:0x1000
.Lf_1239:
	s_waitcnt lgkmcnt(2)
	v_mfma_f32_32x32x64_f8f6f4 v[34:49], v[130:137], v[162:169], v[34:49]
	ds_read_b128 v[162:165], v196 offset:0x1800
	ds_read_b128 v[166:169], v197 offset:0x1800
	v_exp_f32_e32 v98, v98
	v_exp_f32_e32 v99, v99
	v_exp_f32_e32 v100, v100
	v_exp_f32_e32 v101, v101
	v_exp_f32_e32 v102, v102
	v_exp_f32_e32 v103, v103
	v_exp_f32_e32 v104, v104
	v_exp_f32_e32 v105, v105
	v_exp_f32_e32 v106, v106
	v_exp_f32_e32 v107, v107
	v_exp_f32_e32 v108, v108
	s_waitcnt lgkmcnt(2)
	v_mfma_f32_32x32x64_f8f6f4 v[50:65], v[130:137], v[138:145], v[50:65]
	v_exp_f32_e32 v109, v109
	v_exp_f32_e32 v110, v110
	v_exp_f32_e32 v111, v111
	v_exp_f32_e32 v112, v112
	v_exp_f32_e32 v113, v113
	v_exp_f32_e32 v114, v114
	v_exp_f32_e32 v115, v115
	v_exp_f32_e32 v116, v116
	v_exp_f32_e32 v117, v117
	v_exp_f32_e32 v118, v118
	v_exp_f32_e32 v119, v119
	s_waitcnt lgkmcnt(0)
	v_mfma_f32_32x32x64_f8f6f4 v[66:81], v[130:137], v[162:169], v[66:81]
	v_exp_f32_e32 v120, v120
	v_exp_f32_e32 v121, v121
	v_exp_f32_e32 v122, v122
	v_exp_f32_e32 v123, v123
	v_exp_f32_e32 v124, v124
	v_exp_f32_e32 v125, v125
	v_exp_f32_e32 v126, v126
	v_exp_f32_e32 v127, v127
	v_exp_f32_e32 v128, v128
	v_exp_f32_e32 v129, v129
	s_branch .Lf_1214

.LBB0_1264:
	s_lshl_b32 s94, s77, 8
	s_add_i32 s77, s94, 0x8000
	s_and_b64 vcc, exec, s[38:39]
	s_cbranch_vccz .LBB0_1317
	ds_read_b128 v[18:21], v183 offset:0
	ds_read_b128 v[22:25], v190 offset:0
	ds_read_b128 v[34:37], v183 offset:0x800
	ds_read_b128 v[38:41], v190 offset:0x800
	s_waitcnt lgkmcnt(0)
	s_waitcnt vmcnt(0)
	s_nop 9
	v_mfma_f32_32x32x64_f8f6f4 v[18:33], v[18:25], v[154:161], 0
	s_mov_b32 s37, s36
	s_mov_b32 s38, s36
	s_mov_b32 s39, s36
	s_mov_b32 s40, s36
	s_mov_b32 s41, s36
	s_mov_b32 s42, s36
	s_mov_b32 s43, s36
	s_mov_b32 s44, s36
	s_mov_b32 s45, s36
	s_mov_b32 s46, s36
	s_mov_b32 s47, s36
	s_mov_b32 s48, s36
	s_mov_b32 s49, s36
	s_mov_b32 s50, s36
	s_mov_b32 s51, s36
	v_mov_b64_e32 v[2:3], s[36:37]
	v_mov_b64_e32 v[4:5], s[38:39]
	v_mov_b64_e32 v[6:7], s[40:41]
	v_mov_b64_e32 v[8:9], s[42:43]
	v_mov_b64_e32 v[10:11], s[44:45]
	v_mov_b64_e32 v[12:13], s[46:47]
	v_mov_b64_e32 v[14:15], s[48:49]
	v_mov_b64_e32 v[16:17], s[50:51]
	v_max_f32_e32 v42, v19, v19
	v_max_f32_e32 v43, v18, v18
	v_max_f32_e32 v42, v43, v42
	v_max3_f32 v42, v42, v20, v21
	v_max3_f32 v42, v42, v22, v23
	v_max3_f32 v42, v42, v24, v25
	v_max3_f32 v42, v42, v26, v27
	v_max3_f32 v42, v42, v28, v29
	v_max3_f32 v50, v42, v30, v31
	v_mfma_f32_32x32x64_f8f6f4 v[34:49], v[34:41], v[154:161], 0
	v_max3_f32 v50, v50, v32, v33
	s_lshl_b32 s45, s81, 10
	s_lshl_b32 s46, s80, 10
	s_cmp_lg_u32 0, -1
	s_cselect_b32 s38, 0, 0
	s_add_i32 s37, s38, 0x2000
	s_add_i32 s39, s38, 0x3000
	s_add_i32 s6, s38, 0x1000
	v_add_u32_e32 v203, s37, v194
	s_add_i32 s37, s38, 0x6000
	v_add_u32_e32 v199, s39, v194
	s_add_i32 s39, s38, 0x8000
	s_add_i32 s38, s38, 0xa000
	v_add_u32_e32 v205, s6, v194
	v_add_u32_e32 v201, s37, v194
	s_nop 4
	v_max3_f32 v50, v50, v34, v35
	v_max3_f32 v50, v50, v36, v37
	v_max3_f32 v50, v50, v38, v39
	v_max3_f32 v50, v50, v40, v41
	v_max3_f32 v50, v50, v42, v43
	v_max3_f32 v50, v50, v44, v45
	v_max3_f32 v50, v50, v46, v47
	v_max3_f32 v50, v50, v48, v49
	v_mov_b32_e32 v51, v50
	s_nop 1
	v_permlane32_swap_b32_e32 v50, v51
	v_max_f32_e32 v51, v51, v51
	v_max_f32_e32 v50, v50, v50
	v_max_f32_e32 v50, v50, v51
	s_cmp_eq_u32 s98, 0
	s_cselect_b32 s100, 0x40000000, 0xc0600000
	v_add_f32_e32 v198, s100, v50
	v_add_u32_e32 v196, s39, v194
	v_add_u32_e32 v194, s38, v194
	s_lshl_b32 s38, s95, 4
	v_sub_f32_e32 v18, v18, v198
	s_and_b32 s38, s38, 0xfffffc00
	s_ashr_i32 s89, s88, 31
	v_exp_f32_e32 v114, v18
	s_or_b32 s40, s88, 0x100
	s_add_i32 s41, s94, 0x4100
	s_or_b32 s42, s88, 0x140
	s_add_i32 s43, s94, 0x4140
	v_lshl_or_b32 v18, v193, 4, s38
	s_lshl_b64 s[38:39], s[88:89], 10
	s_add_u32 s38, s38, s87
	v_xor_b32_e32 v82, 0x80000000, v198
	v_sub_f32_e32 v34, v34, v198
	v_sub_f32_e32 v19, v19, v198
	v_sub_f32_e32 v35, v35, v198
	v_sub_f32_e32 v20, v20, v198
	v_sub_f32_e32 v36, v36, v198
	v_sub_f32_e32 v21, v21, v198
	v_sub_f32_e32 v37, v37, v198
	v_sub_f32_e32 v22, v22, v198
	v_sub_f32_e32 v38, v38, v198
	v_sub_f32_e32 v23, v23, v198
	v_sub_f32_e32 v39, v39, v198
	v_sub_f32_e32 v24, v24, v198
	v_sub_f32_e32 v40, v40, v198
	v_sub_f32_e32 v25, v25, v198
	v_sub_f32_e32 v41, v41, v198
	v_sub_f32_e32 v26, v26, v198
	v_sub_f32_e32 v42, v42, v198
	v_sub_f32_e32 v27, v27, v198
	v_sub_f32_e32 v43, v43, v198
	v_sub_f32_e32 v28, v28, v198
	v_sub_f32_e32 v44, v44, v198
	v_sub_f32_e32 v29, v29, v198
	v_sub_f32_e32 v45, v45, v198
	v_sub_f32_e32 v30, v30, v198
	v_sub_f32_e32 v46, v46, v198
	v_sub_f32_e32 v31, v31, v198
	v_sub_f32_e32 v47, v47, v198
	v_sub_f32_e32 v32, v32, v198
	v_sub_f32_e32 v48, v48, v198
	v_sub_f32_e32 v33, v33, v198
	v_sub_f32_e32 v49, v49, v198
	s_addc_u32 s39, s39, s76
	v_mov_b32_e32 v83, v82
	v_mov_b32_e32 v84, v82
	v_mov_b32_e32 v85, v82
	v_mov_b32_e32 v86, v82
	v_mov_b32_e32 v87, v82
	v_mov_b32_e32 v88, v82
	v_mov_b32_e32 v89, v82
	v_mov_b32_e32 v90, v82
	v_mov_b32_e32 v91, v82
	v_mov_b32_e32 v92, v82
	v_mov_b32_e32 v93, v82
	v_mov_b32_e32 v94, v82
	v_mov_b32_e32 v95, v82
	v_mov_b32_e32 v96, v82
	v_mov_b32_e32 v97, v82
	v_exp_f32_e32 v98, v34
	v_exp_f32_e32 v115, v19
	v_exp_f32_e32 v99, v35
	v_exp_f32_e32 v116, v20
	v_exp_f32_e32 v100, v36
	v_exp_f32_e32 v117, v21
	v_exp_f32_e32 v101, v37
	v_exp_f32_e32 v118, v22
	v_exp_f32_e32 v102, v38
	v_exp_f32_e32 v119, v23
	v_exp_f32_e32 v103, v39
	v_exp_f32_e32 v120, v24
	v_exp_f32_e32 v104, v40
	v_exp_f32_e32 v121, v25
	v_exp_f32_e32 v105, v41
	v_exp_f32_e32 v122, v26
	v_exp_f32_e32 v106, v42
	v_exp_f32_e32 v123, v27
	v_exp_f32_e32 v107, v43
	v_exp_f32_e32 v124, v28
	v_exp_f32_e32 v108, v44
	v_exp_f32_e32 v125, v29
	v_exp_f32_e32 v109, v45
	v_exp_f32_e32 v126, v30
	v_exp_f32_e32 v110, v46
	v_exp_f32_e32 v127, v31
	v_exp_f32_e32 v111, v47
	v_exp_f32_e32 v128, v32
	v_exp_f32_e32 v112, v48
	v_exp_f32_e32 v129, v33
	v_exp_f32_e32 v113, v49
	v_mov_b32_e32 v19, v181
	s_add_u32 s38, s38, 0x29c30000
	s_waitcnt vmcnt(3) lgkmcnt(0)
	s_barrier
	v_lshl_add_u64 v[172:173], s[92:93], 0, v[18:19]
	s_addc_u32 s39, s39, 0
	v_add3_u32 v18, s79, v191, v192
	v_lshl_add_u64 v[174:175], s[38:39], 0, v[18:19]
	v_mov_b32_e32 v162, 0
	v_mov_b64_e32 v[48:49], v[16:17]
	v_mov_b64_e32 v[64:65], v[16:17]
	v_mov_b64_e32 v[80:81], v[16:17]
	v_mov_b64_e32 v[32:33], v[16:17]
	v_lshl_add_u64 v[170:171], s[28:29], 0, v[180:181]
	v_add_u32_e32 v206, v205, v195
	v_cmp_gt_u32_e64 s[6:7], 32, v193
	v_add_u32_e32 v204, v203, v195
	v_add_u32_e32 v202, v201, v195
	s_movk_i32 s37, 0x100
	v_add_u32_e32 v200, v199, v195
	v_add_u32_e32 v197, v196, v195
	v_add_u32_e32 v195, v194, v195
	s_mov_b32 s44, -3
	s_add_i32 s45, s45, 0
	s_add_i32 s46, s46, 0
	v_mov_b64_e32 v[46:47], v[14:15]
	v_mov_b64_e32 v[44:45], v[12:13]
	v_mov_b64_e32 v[42:43], v[10:11]
	v_mov_b64_e32 v[40:41], v[8:9]
	v_mov_b64_e32 v[38:39], v[6:7]
	v_mov_b64_e32 v[36:37], v[4:5]
	v_mov_b64_e32 v[34:35], v[2:3]
	v_mov_b64_e32 v[62:63], v[14:15]
	v_mov_b64_e32 v[60:61], v[12:13]
	v_mov_b64_e32 v[58:59], v[10:11]
	v_mov_b64_e32 v[56:57], v[8:9]
	v_mov_b64_e32 v[54:55], v[6:7]
	v_mov_b64_e32 v[52:53], v[4:5]
	v_mov_b64_e32 v[50:51], v[2:3]
	v_mov_b64_e32 v[78:79], v[14:15]
	v_mov_b64_e32 v[76:77], v[12:13]
	v_mov_b64_e32 v[74:75], v[10:11]
	v_mov_b64_e32 v[72:73], v[8:9]
	v_mov_b64_e32 v[70:71], v[6:7]
	v_mov_b64_e32 v[68:69], v[4:5]
	v_mov_b64_e32 v[66:67], v[2:3]
	v_mov_b64_e32 v[30:31], v[14:15]
	v_mov_b64_e32 v[28:29], v[12:13]
	v_mov_b64_e32 v[26:27], v[10:11]
	v_mov_b64_e32 v[24:25], v[8:9]
	v_mov_b64_e32 v[22:23], v[6:7]
	v_mov_b64_e32 v[20:21], v[4:5]
	v_mov_b64_e32 v[18:19], v[2:3]
	v_mov_b32_e32 v163, v162
	v_mov_b32_e32 v164, v162
	v_mov_b32_e32 v165, v162
	v_mov_b32_e32 v166, v162
	v_mov_b32_e32 v167, v162
	v_mov_b32_e32 v168, v162
	v_mov_b32_e32 v169, v162
	s_cmp_lg_u32 s98, 0
	s_cbranch_scc1 .LBB0_1268
	s_branch .Lf_1268

.LBB0_1292:
	s_waitcnt lgkmcnt(2)
	v_mfma_f32_32x32x64_f8f6f4 v[34:49], v[162:169], v[138:145], v[34:49]
	ds_read_b128 v[138:141], v194 offset:0x1800
	ds_read_b128 v[142:145], v195 offset:0x1800
	v_exp_f32_e32 v114, v114
	v_exp_f32_e32 v115, v115
	v_exp_f32_e32 v116, v116
	v_exp_f32_e32 v117, v117
	v_exp_f32_e32 v118, v118
	v_exp_f32_e32 v119, v119
	v_exp_f32_e32 v120, v120
	v_exp_f32_e32 v121, v121
	v_exp_f32_e32 v122, v122
	v_exp_f32_e32 v123, v123
	v_exp_f32_e32 v124, v124
	s_waitcnt lgkmcnt(2)
	v_mfma_f32_32x32x64_f8f6f4 v[50:65], v[162:169], v[130:137], v[50:65]
	v_exp_f32_e32 v125, v125
	v_exp_f32_e32 v126, v126
	v_exp_f32_e32 v127, v127
	v_exp_f32_e32 v128, v128
	v_exp_f32_e32 v129, v129
	v_exp_f32_e32 v98, v98
	v_exp_f32_e32 v99, v99
	v_exp_f32_e32 v100, v100
	v_exp_f32_e32 v101, v101
	v_exp_f32_e32 v102, v102
	v_exp_f32_e32 v103, v103
	s_waitcnt lgkmcnt(0)
	v_mfma_f32_32x32x64_f8f6f4 v[66:81], v[162:169], v[138:145], v[66:81]
	v_exp_f32_e32 v104, v104
	v_exp_f32_e32 v105, v105
	v_exp_f32_e32 v106, v106
	v_exp_f32_e32 v107, v107
	v_exp_f32_e32 v108, v108
	v_exp_f32_e32 v109, v109
	v_exp_f32_e32 v110, v110
	v_exp_f32_e32 v111, v111
	v_exp_f32_e32 v112, v112
	v_exp_f32_e32 v113, v113
	s_andn2_b64 vcc, exec, s[38:39]
	s_cbranch_vccnz .LBB0_1267
	s_and_saveexec_b64 s[38:39], s[6:7]
	s_cbranch_execz .LBB0_1266
	ds_write_b32 v187, v176 offset:49152
	s_branch .LBB0_1266
.Lf_1267:
	s_waitcnt vmcnt(3) lgkmcnt(0)
	s_barrier
	s_addk_i32 s37, 0x100
	v_lshl_add_u64 v[172:173], v[172:173], 0, s[72:73]
	s_cmpk_lt_u32 s44, 0xfa
	v_lshl_add_u64 v[174:175], v[174:175], 0, s[74:75]
	s_cbranch_scc0 .LBB0_1295
.Lf_1268:
	s_add_i32 s49, s45, 0x3000
	v_lshl_add_u64 v[130:131], s[14:15], 0, v[174:175]
	s_mov_b32 m0, s49
	v_lshl_add_u64 v[176:177], s[14:15], 0, v[172:173]
	s_add_i32 s47, s46, 0x8000
	global_load_lds_dwordx4 v[130:131], off
	v_lshl_add_u64 v[130:131], v[176:177], 0, s[56:57]
	s_mov_b32 m0, s47
	s_add_i32 s48, s46, 0x9000
	global_load_lds_dwordx4 v[130:131], off
	v_lshl_add_u64 v[130:131], v[176:177], 0, s[58:59]
	s_mov_b32 m0, s48
	v_cvt_pk_fp8_f32 v162, v114, v115
	global_load_lds_dwordx4 v[130:131], off
	v_cvt_pk_fp8_f32 v163, v118, v119
	ds_read_b128 v[130:133], v205 offset:0
	ds_read_b128 v[134:137], v206 offset:0
	ds_read_b128 v[210:213], v205 offset:0x800
	ds_read_b128 v[214:217], v206 offset:0x800
	v_cvt_pk_fp8_f32 v162, v116, v117 op_sel:[0,0,1]
	v_cvt_pk_fp8_f32 v163, v120, v121 op_sel:[0,0,1]
	s_waitcnt lgkmcnt(2)
	v_cvt_pk_fp8_f32 v164, v122, v123
	v_cvt_pk_fp8_f32 v165, v126, v127
	ds_read_b128 v[218:221], v188 offset:0
	ds_read_b128 v[222:225], v189 offset:0
	v_cvt_pk_fp8_f32 v164, v124, v125 op_sel:[0,0,1]
	v_cvt_pk_fp8_f32 v165, v128, v129 op_sel:[0,0,1]
	v_mfma_f32_32x32x64_f8f6f4 v[114:129], v[130:137], v[154:161], v[82:97]
	s_waitcnt lgkmcnt(2)
	v_mfma_f32_32x32x64_f8f6f4 v[130:145], v[210:217], v[154:161], v[82:97]
	v_cvt_pk_fp8_f32 v166, v98, v99
	v_cvt_pk_fp8_f32 v167, v102, v103
	v_cvt_pk_fp8_f32 v168, v106, v107
	v_cvt_pk_fp8_f32 v169, v110, v111
	v_cvt_pk_fp8_f32 v166, v100, v101 op_sel:[0,0,1]
	v_cvt_pk_fp8_f32 v167, v104, v105 op_sel:[0,0,1]
	v_cvt_pk_fp8_f32 v168, v108, v109 op_sel:[0,0,1]
	v_cvt_pk_fp8_f32 v169, v112, v113 op_sel:[0,0,1]
	s_nop 0
	ds_read_b128 v[106:109], v188 offset:0x800
	ds_read_b128 v[110:113], v189 offset:0x800
	s_nop 0
	v_mfma_f32_16x16x128_f8f6f4 v[18:21], v[162:169], v[146:153], v[18:21]
	s_waitcnt lgkmcnt(2)
	v_mfma_f32_32x32x64_f8f6f4 v[2:17], v[162:169], v[218:225], v[2:17]
	ds_read_b128 v[98:101], v188 offset:0x1000
	ds_read_b128 v[102:105], v189 offset:0x1000
.Lf_1271:
	s_waitcnt lgkmcnt(2)
	v_mfma_f32_32x32x64_f8f6f4 v[34:49], v[162:169], v[106:113], v[34:49]
	ds_read_b128 v[106:109], v188 offset:0x1800
	ds_read_b128 v[110:113], v189 offset:0x1800
	v_exp_f32_e32 v114, v114
	v_exp_f32_e32 v115, v115
	v_exp_f32_e32 v116, v116
	v_exp_f32_e32 v117, v117
	v_exp_f32_e32 v118, v118
	v_exp_f32_e32 v119, v119
	v_exp_f32_e32 v120, v120
	v_exp_f32_e32 v121, v121
	v_exp_f32_e32 v122, v122
	v_exp_f32_e32 v123, v123
	v_exp_f32_e32 v124, v124
	s_waitcnt lgkmcnt(2)
	v_mfma_f32_32x32x64_f8f6f4 v[50:65], v[162:169], v[98:105], v[50:65]
	v_exp_f32_e32 v125, v125
	v_exp_f32_e32 v126, v126
	v_exp_f32_e32 v127, v127
	v_exp_f32_e32 v128, v128
	v_exp_f32_e32 v129, v129
	v_exp_f32_e32 v130, v130
	v_exp_f32_e32 v131, v131
	v_exp_f32_e32 v132, v132
	v_exp_f32_e32 v133, v133
	v_exp_f32_e32 v134, v134
	v_exp_f32_e32 v135, v135
	s_waitcnt lgkmcnt(0)
	v_mfma_f32_32x32x64_f8f6f4 v[66:81], v[162:169], v[106:113], v[66:81]
	v_exp_f32_e32 v136, v136
	v_exp_f32_e32 v137, v137
	v_exp_f32_e32 v138, v138
	v_exp_f32_e32 v139, v139
	v_exp_f32_e32 v140, v140
	v_exp_f32_e32 v141, v141
	v_exp_f32_e32 v142, v142
	v_exp_f32_e32 v143, v143
	v_exp_f32_e32 v144, v144
	v_exp_f32_e32 v145, v145
.Lf_1275:
	s_add_i32 s38, s88, s37
	s_cmpk_eq_i32 s44, 0xf9
	s_cselect_b32 s38, s77, s38
	s_ashr_i32 s39, s38, 31
	s_lshl_b64 s[38:39], s[38:39], 10
	s_mov_b32 m0, s45
	s_waitcnt vmcnt(3) lgkmcnt(0)
	s_barrier
	v_lshl_add_u64 v[98:99], v[170:171], 0, s[38:39]
	s_add_i32 s51, s46, 0xa000
	global_load_lds_dwordx4 v[98:99], off
	v_lshl_add_u64 v[98:99], v[176:177], 0, s[60:61]
	s_mov_b32 m0, s51
	s_add_i32 s50, s46, 0xb000
	global_load_lds_dwordx4 v[98:99], off
	v_lshl_add_u64 v[98:99], v[176:177], 0, s[62:63]
	s_mov_b32 m0, s50
	v_cvt_pk_fp8_f32 v162, v114, v115
	global_load_lds_dwordx4 v[98:99], off
	v_cvt_pk_fp8_f32 v163, v118, v119
	ds_read_b128 v[210:213], v203 offset:0
	ds_read_b128 v[214:217], v204 offset:0
	ds_read_b128 v[218:221], v203 offset:0x800
	ds_read_b128 v[222:225], v204 offset:0x800
	v_cvt_pk_fp8_f32 v162, v116, v117 op_sel:[0,0,1]
	v_cvt_pk_fp8_f32 v163, v120, v121 op_sel:[0,0,1]
	s_waitcnt lgkmcnt(2)
	v_mfma_f32_32x32x64_f8f6f4 v[98:113], v[210:217], v[154:161], v[82:97]
	v_cvt_pk_fp8_f32 v164, v122, v123
	v_cvt_pk_fp8_f32 v165, v126, v127
	ds_read_b128 v[226:229], v201 offset:0
	ds_read_b128 v[230:233], v202 offset:0
	v_cvt_pk_fp8_f32 v164, v124, v125 op_sel:[0,0,1]
	v_cvt_pk_fp8_f32 v165, v128, v129 op_sel:[0,0,1]
	s_waitcnt lgkmcnt(2)
	v_mfma_f32_32x32x64_f8f6f4 v[114:129], v[218:225], v[154:161], v[82:97]
	v_cvt_pk_fp8_f32 v166, v130, v131
	v_cvt_pk_fp8_f32 v167, v134, v135
	v_cvt_pk_fp8_f32 v168, v138, v139
	v_cvt_pk_fp8_f32 v169, v142, v143
	v_cvt_pk_fp8_f32 v166, v132, v133 op_sel:[0,0,1]
	v_cvt_pk_fp8_f32 v167, v136, v137 op_sel:[0,0,1]
	v_cvt_pk_fp8_f32 v168, v140, v141 op_sel:[0,0,1]
	v_cvt_pk_fp8_f32 v169, v144, v145 op_sel:[0,0,1]
	s_nop 0
	ds_read_b128 v[138:141], v201 offset:0x800
	ds_read_b128 v[142:145], v202 offset:0x800
	s_nop 0
	v_mfma_f32_16x16x128_f8f6f4 v[18:21], v[162:169], v[146:153], v[18:21]
	s_waitcnt lgkmcnt(2)
	v_mfma_f32_32x32x64_f8f6f4 v[2:17], v[162:169], v[226:233], v[2:17]
	ds_read_b128 v[130:133], v201 offset:0x1000
	ds_read_b128 v[134:137], v202 offset:0x1000
.Lf_1278:
	s_waitcnt lgkmcnt(2)
	v_mfma_f32_32x32x64_f8f6f4 v[34:49], v[162:169], v[138:145], v[34:49]
	ds_read_b128 v[138:141], v201 offset:0x1800
	ds_read_b128 v[142:145], v202 offset:0x1800
	v_exp_f32_e32 v98, v98
	v_exp_f32_e32 v99, v99
	v_exp_f32_e32 v100, v100
	v_exp_f32_e32 v101, v101
	v_exp_f32_e32 v102, v102
	v_exp_f32_e32 v103, v103
	v_exp_f32_e32 v104, v104
	v_exp_f32_e32 v105, v105
	v_exp_f32_e32 v106, v106
	v_exp_f32_e32 v107, v107
	v_exp_f32_e32 v108, v108
	s_waitcnt lgkmcnt(2)
	v_mfma_f32_32x32x64_f8f6f4 v[50:65], v[162:169], v[130:137], v[50:65]
	v_exp_f32_e32 v109, v109
	v_exp_f32_e32 v110, v110
	v_exp_f32_e32 v111, v111
	v_exp_f32_e32 v112, v112
	v_exp_f32_e32 v113, v113
	v_exp_f32_e32 v114, v114
	v_exp_f32_e32 v115, v115
	v_exp_f32_e32 v116, v116
	v_exp_f32_e32 v117, v117
	v_exp_f32_e32 v118, v118
	v_exp_f32_e32 v119, v119
	s_waitcnt lgkmcnt(0)
	v_mfma_f32_32x32x64_f8f6f4 v[66:81], v[162:169], v[138:145], v[66:81]
	v_exp_f32_e32 v120, v120
	v_exp_f32_e32 v121, v121
	v_exp_f32_e32 v122, v122
	v_exp_f32_e32 v123, v123
	v_exp_f32_e32 v124, v124
	v_exp_f32_e32 v125, v125
	v_exp_f32_e32 v126, v126
	v_exp_f32_e32 v127, v127
	v_exp_f32_e32 v128, v128
	v_exp_f32_e32 v129, v129
.Lf_1282:
	s_add_i32 s44, s44, 4
	s_cmpk_lt_u32 s44, 0xfc
	s_cselect_b32 s38, s40, s41
	s_add_i32 s38, s38, s37
	s_addk_i32 s38, 0xff40
	s_ashr_i32 s39, s38, 31
	s_lshl_b64 s[38:39], s[38:39], 10
	s_waitcnt vmcnt(3) lgkmcnt(0)
	s_barrier
	v_lshl_add_u64 v[130:131], v[170:171], 0, s[38:39]
	s_add_i32 m0, s45, 0x1000
	v_cvt_pk_fp8_f32 v162, v98, v99
	global_load_lds_dwordx4 v[130:131], off
	v_lshl_add_u64 v[130:131], v[176:177], 0, s[64:65]
	s_add_i32 m0, s46, 0x4000
	v_cvt_pk_fp8_f32 v163, v102, v103
	global_load_lds_dwordx4 v[130:131], off
	v_lshl_add_u64 v[130:131], v[176:177], 0, s[66:67]
	s_add_i32 m0, s46, 0x5000
	v_cvt_pk_fp8_f32 v162, v100, v101 op_sel:[0,0,1]
	global_load_lds_dwordx4 v[130:131], off
	ds_read_b128 v[130:133], v199 offset:0
	ds_read_b128 v[134:137], v200 offset:0
	ds_read_b128 v[210:213], v199 offset:0x800
	ds_read_b128 v[214:217], v200 offset:0x800
	v_cvt_pk_fp8_f32 v163, v104, v105 op_sel:[0,0,1]
	s_waitcnt lgkmcnt(2)
	v_cvt_pk_fp8_f32 v164, v106, v107
	v_cvt_pk_fp8_f32 v165, v110, v111
	ds_read_b128 v[218:221], v196 offset:0
	ds_read_b128 v[222:225], v197 offset:0
	v_cvt_pk_fp8_f32 v164, v108, v109 op_sel:[0,0,1]
	v_cvt_pk_fp8_f32 v165, v112, v113 op_sel:[0,0,1]
	v_mfma_f32_32x32x64_f8f6f4 v[98:113], v[130:137], v[154:161], v[82:97]
	s_waitcnt lgkmcnt(2)
	v_mfma_f32_32x32x64_f8f6f4 v[130:145], v[210:217], v[154:161], v[82:97]
	v_cvt_pk_fp8_f32 v166, v114, v115
	v_cvt_pk_fp8_f32 v167, v118, v119
	v_cvt_pk_fp8_f32 v168, v122, v123
	v_cvt_pk_fp8_f32 v169, v126, v127
	v_cvt_pk_fp8_f32 v166, v116, v117 op_sel:[0,0,1]
	v_cvt_pk_fp8_f32 v167, v120, v121 op_sel:[0,0,1]
	v_cvt_pk_fp8_f32 v168, v124, v125 op_sel:[0,0,1]
	v_cvt_pk_fp8_f32 v169, v128, v129 op_sel:[0,0,1]
	s_nop 0
	ds_read_b128 v[122:125], v196 offset:0x800
	ds_read_b128 v[126:129], v197 offset:0x800
	s_nop 0
	v_mfma_f32_16x16x128_f8f6f4 v[18:21], v[162:169], v[146:153], v[18:21]
	s_waitcnt lgkmcnt(2)
	v_mfma_f32_32x32x64_f8f6f4 v[2:17], v[162:169], v[218:225], v[2:17]
	ds_read_b128 v[114:117], v196 offset:0x1000
	ds_read_b128 v[118:121], v197 offset:0x1000
.Lf_1285:
	s_waitcnt lgkmcnt(2)
	v_mfma_f32_32x32x64_f8f6f4 v[34:49], v[162:169], v[122:129], v[34:49]
	ds_read_b128 v[122:125], v196 offset:0x1800
	ds_read_b128 v[126:129], v197 offset:0x1800
	v_exp_f32_e32 v98, v98
	v_exp_f32_e32 v99, v99
	v_exp_f32_e32 v100, v100
	v_exp_f32_e32 v101, v101
	v_exp_f32_e32 v102, v102
	v_exp_f32_e32 v103, v103
	v_exp_f32_e32 v104, v104
	v_exp_f32_e32 v105, v105
	v_exp_f32_e32 v106, v106
	v_exp_f32_e32 v107, v107
	v_exp_f32_e32 v108, v108
	s_waitcnt lgkmcnt(2)
	v_mfma_f32_32x32x64_f8f6f4 v[50:65], v[162:169], v[114:121], v[50:65]
	v_exp_f32_e32 v109, v109
	v_exp_f32_e32 v110, v110
	v_exp_f32_e32 v111, v111
	v_exp_f32_e32 v112, v112
	v_exp_f32_e32 v113, v113
	v_exp_f32_e32 v130, v130
	v_exp_f32_e32 v131, v131
	v_exp_f32_e32 v132, v132
	v_exp_f32_e32 v133, v133
	v_exp_f32_e32 v134, v134
	v_exp_f32_e32 v135, v135
	s_waitcnt lgkmcnt(0)
	v_mfma_f32_32x32x64_f8f6f4 v[66:81], v[162:169], v[122:129], v[66:81]
	v_exp_f32_e32 v136, v136
	v_exp_f32_e32 v137, v137
	v_exp_f32_e32 v138, v138
	v_exp_f32_e32 v139, v139
	v_exp_f32_e32 v140, v140
	v_exp_f32_e32 v141, v141
	v_exp_f32_e32 v142, v142
	v_exp_f32_e32 v143, v143
	v_exp_f32_e32 v144, v144
	v_exp_f32_e32 v145, v145
.Lf_1289:
	s_cmpk_lt_u32 s44, 0xfb
	s_cselect_b32 s38, s42, s43
	s_add_i32 s38, s38, s37
	s_addk_i32 s38, 0xff40
	s_ashr_i32 s39, s38, 31
	s_lshl_b64 s[38:39], s[38:39], 10
	s_waitcnt vmcnt(3) lgkmcnt(0)
	s_barrier
	v_lshl_add_u64 v[114:115], v[170:171], 0, s[38:39]
	s_add_i32 m0, s45, 0x2000
	v_cvt_pk_fp8_f32 v162, v98, v99
	global_load_lds_dwordx4 v[114:115], off
	v_lshl_add_u64 v[114:115], v[176:177], 0, s[68:69]
	s_add_i32 m0, s46, 0x6000
	v_cvt_pk_fp8_f32 v163, v102, v103
	global_load_lds_dwordx4 v[114:115], off
	v_lshl_add_u64 v[114:115], v[176:177], 0, s[70:71]
	s_add_i32 m0, s46, 0x7000
	v_cvt_pk_fp8_f32 v162, v100, v101 op_sel:[0,0,1]
	global_load_lds_dwordx4 v[114:115], off
	ds_read_b128 v[210:213], v183 offset:0
	ds_read_b128 v[214:217], v190 offset:0
	ds_read_b128 v[218:221], v183 offset:0x800
	ds_read_b128 v[222:225], v190 offset:0x800
	v_cvt_pk_fp8_f32 v163, v104, v105 op_sel:[0,0,1]
	s_waitcnt lgkmcnt(2)
	v_mfma_f32_32x32x64_f8f6f4 v[114:129], v[210:217], v[154:161], v[82:97]
	v_cvt_pk_fp8_f32 v164, v106, v107
	v_cvt_pk_fp8_f32 v165, v110, v111
	ds_read_b128 v[226:229], v194 offset:0
	ds_read_b128 v[230:233], v195 offset:0
	v_cvt_pk_fp8_f32 v164, v108, v109 op_sel:[0,0,1]
	v_cvt_pk_fp8_f32 v165, v112, v113 op_sel:[0,0,1]
	s_waitcnt lgkmcnt(2)
	v_mfma_f32_32x32x64_f8f6f4 v[98:113], v[218:225], v[154:161], v[82:97]
	v_cvt_pk_fp8_f32 v166, v130, v131
	v_cvt_pk_fp8_f32 v167, v134, v135
	v_cvt_pk_fp8_f32 v168, v138, v139
	v_cvt_pk_fp8_f32 v169, v142, v143
	v_cvt_pk_fp8_f32 v166, v132, v133 op_sel:[0,0,1]
	v_cvt_pk_fp8_f32 v167, v136, v137 op_sel:[0,0,1]
	v_cvt_pk_fp8_f32 v168, v140, v141 op_sel:[0,0,1]
	v_cvt_pk_fp8_f32 v169, v144, v145 op_sel:[0,0,1]
	s_nop 0
	ds_read_b128 v[138:141], v194 offset:0x800
	ds_read_b128 v[142:145], v195 offset:0x800
	s_nop 0
	v_mfma_f32_16x16x128_f8f6f4 v[18:21], v[162:169], v[146:153], v[18:21]
	s_waitcnt lgkmcnt(2)
	v_mfma_f32_32x32x64_f8f6f4 v[2:17], v[162:169], v[226:233], v[2:17]
	ds_read_b128 v[130:133], v194 offset:0x1000
	ds_read_b128 v[134:137], v195 offset:0x1000
.Lf_1292:
	s_waitcnt lgkmcnt(2)
	v_mfma_f32_32x32x64_f8f6f4 v[34:49], v[162:169], v[138:145], v[34:49]
	ds_read_b128 v[138:141], v194 offset:0x1800
	ds_read_b128 v[142:145], v195 offset:0x1800
	v_exp_f32_e32 v114, v114
	v_exp_f32_e32 v115, v115
	v_exp_f32_e32 v116, v116
	v_exp_f32_e32 v117, v117
	v_exp_f32_e32 v118, v118
	v_exp_f32_e32 v119, v119
	v_exp_f32_e32 v120, v120
	v_exp_f32_e32 v121, v121
	v_exp_f32_e32 v122, v122
	v_exp_f32_e32 v123, v123
	v_exp_f32_e32 v124, v124
	s_waitcnt lgkmcnt(2)
	v_mfma_f32_32x32x64_f8f6f4 v[50:65], v[162:169], v[130:137], v[50:65]
	v_exp_f32_e32 v125, v125
	v_exp_f32_e32 v126, v126
	v_exp_f32_e32 v127, v127
	v_exp_f32_e32 v128, v128
	v_exp_f32_e32 v129, v129
	v_exp_f32_e32 v98, v98
	v_exp_f32_e32 v99, v99
	v_exp_f32_e32 v100, v100
	v_exp_f32_e32 v101, v101
	v_exp_f32_e32 v102, v102
	v_exp_f32_e32 v103, v103
	s_waitcnt lgkmcnt(0)
	v_mfma_f32_32x32x64_f8f6f4 v[66:81], v[162:169], v[138:145], v[66:81]
	v_exp_f32_e32 v104, v104
	v_exp_f32_e32 v105, v105
	v_exp_f32_e32 v106, v106
	v_exp_f32_e32 v107, v107
	v_exp_f32_e32 v108, v108
	v_exp_f32_e32 v109, v109
	v_exp_f32_e32 v110, v110
	v_exp_f32_e32 v111, v111
	v_exp_f32_e32 v112, v112
	v_exp_f32_e32 v113, v113
	s_branch .Lf_1267

.LBB0_1323:
	s_and_b32 s37, s80, 0xffffffc0
	v_lshlrev_b32_e32 v6, 2, v5
	v_lshlrev_b32_e32 v3, 6, v4
	v_and_b32_e32 v6, 48, v6
	s_cmp_lg_u32 0, -1
	v_bitop3_b32 v194, v6, v3, v2 bitop3:0xde
	s_cselect_b32 s38, 0, 0
	v_lshlrev_b32_e32 v2, 3, v5
	v_and_b32_e32 v193, 63, v5
	v_add_u32_e32 v183, s38, v194
	s_addk_i32 s38, 0x4000
	v_and_b32_e32 v2, 32, v2
	s_lshl_b32 s37, s37, 2
	v_add_u32_e32 v188, s38, v194
	v_sub_u32_e32 v195, 16, v2
	v_lshrrev_b32_e32 v2, 5, v193
	s_add_i32 s78, s37, 0
	v_add_u32_e32 v190, v183, v195
	s_mov_b64 s[38:39], -1
	s_and_b64 vcc, exec, s[6:7]
	v_add_u32_e32 v189, v188, v195
	v_cmp_gt_u32_e64 s[6:7], 32, v193
	v_lshlrev_b32_e32 v186, 4, v2
	v_lshl_add_u32 v187, v4, 2, s78
	v_and_b32_e32 v248, 31, v193
	v_mov_b32_e32 v249, 0x38383838
	v_cmp_eq_u32_e64 s[100:101], 0, v248
	v_lshrrev_b32_e32 v250, 4, v193
	s_nop 0
	v_cndmask_b32_e64 v146, 0, v249, s[100:101]
	v_cmp_eq_u32_e64 s[100:101], 17, v248
	v_and_b32_e32 v248, 15, v193
	v_lshlrev_b32_e32 v248, 6, v248
	v_cndmask_b32_e64 v146, v146, v249, s[100:101]
	v_lshl_add_u32 v250, v250, 4, v248
	v_add_u32_e32 v250, s78, v250
	v_mov_b32_e32 v147, v146
	v_mov_b32_e32 v148, v146
	v_mov_b32_e32 v149, v146
	v_mov_b32_e32 v150, v146
	v_mov_b32_e32 v151, v146
	v_mov_b32_e32 v152, v146
	v_mov_b32_e32 v153, v146
	s_cbranch_vccz .LBB0_1376
	ds_read_b128 v[18:21], v183 offset:0
	ds_read_b128 v[22:25], v190 offset:0
	ds_read_b128 v[34:37], v183 offset:0x800
	ds_read_b128 v[38:41], v190 offset:0x800
	s_waitcnt lgkmcnt(0)
	s_waitcnt vmcnt(0)
	v_mfma_f32_32x32x64_f8f6f4 v[18:33], v[18:25], v[154:161], 0
	s_mov_b32 s37, s36
	s_mov_b32 s38, s36
	s_mov_b32 s39, s36
	s_mov_b32 s40, s36
	s_mov_b32 s41, s36
	s_mov_b32 s42, s36
	s_mov_b32 s43, s36
	s_mov_b32 s44, s36
	s_mov_b32 s45, s36
	s_mov_b32 s46, s36
	s_mov_b32 s47, s36
	s_mov_b32 s48, s36
	s_mov_b32 s49, s36
	s_mov_b32 s50, s36
	s_mov_b32 s51, s36
	v_mov_b64_e32 v[2:3], s[36:37]
	v_mov_b64_e32 v[4:5], s[38:39]
	v_mov_b64_e32 v[6:7], s[40:41]
	v_mov_b64_e32 v[8:9], s[42:43]
	v_mov_b64_e32 v[10:11], s[44:45]
	v_mov_b64_e32 v[12:13], s[46:47]
	v_mov_b64_e32 v[14:15], s[48:49]
	v_mov_b64_e32 v[16:17], s[50:51]
	v_max_f32_e32 v42, v19, v19
	v_max_f32_e32 v43, v18, v18
	v_max_f32_e32 v42, v43, v42
	v_max3_f32 v42, v42, v20, v21
	v_max3_f32 v42, v42, v22, v23
	v_max3_f32 v42, v42, v24, v25
	v_max3_f32 v42, v42, v26, v27
	v_max3_f32 v42, v42, v28, v29
	v_max3_f32 v50, v42, v30, v31
	v_mfma_f32_32x32x64_f8f6f4 v[34:49], v[34:41], v[154:161], 0
	v_max3_f32 v50, v50, v32, v33
	s_cmp_lg_u32 0, -1
	s_cselect_b32 s37, 0, 0
	v_mov_b32_e32 v130, v181
	v_mov_b32_e32 v131, v181
	s_add_i32 s38, s37, 0x1000
	s_waitcnt vmcnt(0) lgkmcnt(0)
	s_barrier
	v_add_u32_e32 v207, s38, v194
	v_add_u32_e32 v209, v207, v195
	s_nop 11
	v_max3_f32 v50, v50, v34, v35
	v_max3_f32 v50, v50, v36, v37
	v_max3_f32 v50, v50, v38, v39
	v_max3_f32 v50, v50, v40, v41
	v_max3_f32 v50, v50, v42, v43
	v_max3_f32 v50, v50, v44, v45
	v_max3_f32 v50, v50, v46, v47
	v_max3_f32 v50, v50, v48, v49
	v_mov_b32_e32 v51, v50
	s_nop 1
	v_permlane32_swap_b32_e32 v50, v51
	v_max_f32_e32 v51, v51, v51
	v_max_f32_e32 v50, v50, v50
	v_max_f32_e32 v50, v50, v51
	s_cmp_eq_u32 s98, 0
	s_cselect_b32 s100, 0x40000000, 0xc0600000
	v_add_f32_e32 v198, s100, v50
	v_sub_f32_e32 v18, v18, v198
	v_sub_f32_e32 v19, v19, v198
	v_sub_f32_e32 v22, v22, v198
	v_sub_f32_e32 v23, v23, v198
	v_exp_f32_e32 v50, v18
	v_exp_f32_e32 v51, v19
	v_exp_f32_e32 v54, v22
	v_exp_f32_e32 v55, v23
	v_xor_b32_e32 v82, 0x80000000, v198
	v_sub_f32_e32 v20, v20, v198
	v_sub_f32_e32 v21, v21, v198
	v_sub_f32_e32 v24, v24, v198
	v_sub_f32_e32 v25, v25, v198
	v_mov_b32_e32 v83, v82
	v_mov_b32_e32 v84, v82
	v_mov_b32_e32 v85, v82
	v_mov_b32_e32 v86, v82
	v_mov_b32_e32 v87, v82
	v_mov_b32_e32 v88, v82
	v_mov_b32_e32 v89, v82
	v_mov_b32_e32 v90, v82
	v_mov_b32_e32 v91, v82
	v_mov_b32_e32 v92, v82
	v_mov_b32_e32 v93, v82
	v_mov_b32_e32 v94, v82
	v_mov_b32_e32 v95, v82
	v_mov_b32_e32 v96, v82
	v_mov_b32_e32 v97, v82
	v_exp_f32_e32 v52, v20
	v_exp_f32_e32 v53, v21
	v_exp_f32_e32 v56, v24
	v_exp_f32_e32 v57, v25
	v_cvt_pk_fp8_f32 v130, v50, v51
	v_cvt_pk_fp8_f32 v131, v54, v55
	ds_read_b128 v[18:21], v207 offset:0
	v_sub_f32_e32 v26, v26, v198
	v_sub_f32_e32 v27, v27, v198
	v_sub_f32_e32 v28, v28, v198
	v_sub_f32_e32 v29, v29, v198
	ds_read_b128 v[22:25], v209 offset:0
	v_sub_f32_e32 v34, v34, v198
	v_sub_f32_e32 v35, v35, v198
	v_sub_f32_e32 v36, v36, v198
	v_sub_f32_e32 v37, v37, v198
	v_sub_f32_e32 v38, v38, v198
	v_sub_f32_e32 v39, v39, v198
	v_sub_f32_e32 v40, v40, v198
	v_sub_f32_e32 v41, v41, v198
	v_sub_f32_e32 v42, v42, v198
	v_sub_f32_e32 v43, v43, v198
	v_sub_f32_e32 v44, v44, v198
	v_sub_f32_e32 v45, v45, v198
	v_sub_f32_e32 v30, v30, v198
	v_sub_f32_e32 v46, v46, v198
	v_sub_f32_e32 v31, v31, v198
	v_sub_f32_e32 v47, v47, v198
	v_sub_f32_e32 v32, v32, v198
	v_sub_f32_e32 v48, v48, v198
	v_sub_f32_e32 v33, v33, v198
	v_sub_f32_e32 v49, v49, v198
	v_exp_f32_e32 v58, v26
	v_exp_f32_e32 v59, v27
	v_exp_f32_e32 v60, v28
	v_exp_f32_e32 v61, v29
	ds_read_b128 v[26:29], v207 offset:0x800
	v_exp_f32_e32 v34, v34
	v_exp_f32_e32 v35, v35
	v_exp_f32_e32 v36, v36
	v_exp_f32_e32 v37, v37
	v_exp_f32_e32 v38, v38
	v_exp_f32_e32 v39, v39
	v_exp_f32_e32 v40, v40
	v_exp_f32_e32 v41, v41
	v_exp_f32_e32 v42, v42
	v_exp_f32_e32 v43, v43
	v_exp_f32_e32 v44, v44
	v_exp_f32_e32 v45, v45
	v_exp_f32_e32 v62, v30
	v_exp_f32_e32 v46, v46
	v_exp_f32_e32 v63, v31
	v_exp_f32_e32 v47, v47
	v_exp_f32_e32 v64, v32
	v_exp_f32_e32 v48, v48
	v_exp_f32_e32 v65, v33
	v_exp_f32_e32 v49, v49
	ds_read_b128 v[30:33], v209 offset:0x800
	v_cvt_pk_fp8_f32 v130, v52, v53 op_sel:[0,0,1]
	v_cvt_pk_fp8_f32 v131, v56, v57 op_sel:[0,0,1]
	s_waitcnt lgkmcnt(2)
	v_mfma_f32_32x32x64_f8f6f4 v[98:113], v[18:25], v[154:161], v[82:97]
	v_mov_b32_e32 v132, v181
	v_mov_b32_e32 v133, v181
	v_cvt_pk_fp8_f32 v132, v58, v59
	v_cvt_pk_fp8_f32 v133, v62, v63
	ds_read_b128 v[170:173], v188 offset:0
	ds_read_b128 v[174:177], v189 offset:0
	v_cvt_pk_fp8_f32 v132, v60, v61 op_sel:[0,0,1]
	v_cvt_pk_fp8_f32 v133, v64, v65 op_sel:[0,0,1]
	s_waitcnt lgkmcnt(2)
	v_mov_b64_e32 v[128:129], v[96:97]
	v_mov_b64_e32 v[126:127], v[94:95]
	v_mov_b64_e32 v[124:125], v[92:93]
	v_mov_b64_e32 v[122:123], v[90:91]
	v_mov_b64_e32 v[120:121], v[88:89]
	v_mov_b64_e32 v[118:119], v[86:87]
	v_mov_b64_e32 v[116:117], v[84:85]
	v_mov_b64_e32 v[114:115], v[82:83]
	v_mov_b32_e32 v134, v181
	v_mov_b32_e32 v135, v181
	v_mfma_f32_32x32x64_f8f6f4 v[114:129], v[26:33], v[154:161], v[114:129]
	v_mov_b32_e32 v136, v181
	v_mov_b32_e32 v137, v181
	v_cvt_pk_fp8_f32 v134, v34, v35
	v_cvt_pk_fp8_f32 v135, v38, v39
	v_cvt_pk_fp8_f32 v136, v42, v43
	v_cvt_pk_fp8_f32 v137, v46, v47
	v_cvt_pk_fp8_f32 v134, v36, v37 op_sel:[0,0,1]
	v_cvt_pk_fp8_f32 v135, v40, v41 op_sel:[0,0,1]
	v_cvt_pk_fp8_f32 v136, v44, v45 op_sel:[0,0,1]
	v_cvt_pk_fp8_f32 v137, v48, v49 op_sel:[0,0,1]
	s_nop 0
	ds_read_b128 v[138:141], v188 offset:0x800
	ds_read_b128 v[142:145], v189 offset:0x800
	s_nop 0
	v_mfma_f32_16x16x128_f8f6f4 v[18:21], v[130:137], v[146:153], 0
	s_add_i32 s38, s37, 0x2000
	v_add_u32_e32 v205, s38, v194
	s_add_i32 s38, s37, 0x6000
	v_add_u32_e32 v203, s38, v194
	s_add_i32 s38, s37, 0x3000
	s_waitcnt vmcnt(0) lgkmcnt(0)
	s_barrier
	v_add_u32_e32 v201, s38, v194
	s_add_i32 s38, s37, 0x8000
	s_add_i32 s37, s37, 0xa000
	v_add_u32_e32 v199, s38, v194
	v_add_u32_e32 v196, s37, v194
	v_mov_b64_e32 v[48:49], v[16:17]
	v_mov_b64_e32 v[64:65], v[16:17]
	v_mov_b64_e32 v[80:81], v[16:17]
	v_add_u32_e32 v206, v205, v195
	v_add_u32_e32 v204, v203, v195
	v_add_u32_e32 v202, v201, v195
	v_add_u32_e32 v200, v199, v195
	v_add_u32_e32 v197, v196, v195
	s_mov_b32 s37, -2
	v_mov_b64_e32 v[46:47], v[14:15]
	v_mov_b64_e32 v[44:45], v[12:13]
	v_mov_b64_e32 v[42:43], v[10:11]
	v_mov_b64_e32 v[40:41], v[8:9]
	v_mov_b64_e32 v[38:39], v[6:7]
	v_mov_b64_e32 v[36:37], v[4:5]
	v_mov_b64_e32 v[34:35], v[2:3]
	v_mov_b64_e32 v[62:63], v[14:15]
	v_mov_b64_e32 v[60:61], v[12:13]
	v_mov_b64_e32 v[58:59], v[10:11]
	v_mov_b64_e32 v[56:57], v[8:9]
	v_mov_b64_e32 v[54:55], v[6:7]
	v_mov_b64_e32 v[52:53], v[4:5]
	v_mov_b64_e32 v[50:51], v[2:3]
	v_mov_b64_e32 v[78:79], v[14:15]
	v_mov_b64_e32 v[76:77], v[12:13]
	v_mov_b64_e32 v[74:75], v[10:11]
	v_mov_b64_e32 v[72:73], v[8:9]
	v_mov_b64_e32 v[70:71], v[6:7]
	v_mov_b64_e32 v[68:69], v[4:5]
	v_mov_b64_e32 v[66:67], v[2:3]
	s_cmp_lg_u32 s98, 0
	s_cbranch_scc1 .LBB0_1327
	s_branch .Lf_1327

.LBB0_1351:
	s_waitcnt lgkmcnt(2)
	v_mfma_f32_32x32x64_f8f6f4 v[34:49], v[130:137], v[162:169], v[34:49]
	ds_read_b128 v[162:165], v196 offset:0x1800
	ds_read_b128 v[166:169], v197 offset:0x1800
	v_exp_f32_e32 v98, v98
	v_exp_f32_e32 v99, v99
	v_exp_f32_e32 v100, v100
	v_exp_f32_e32 v101, v101
	v_exp_f32_e32 v102, v102
	v_exp_f32_e32 v103, v103
	v_exp_f32_e32 v104, v104
	v_exp_f32_e32 v105, v105
	v_exp_f32_e32 v106, v106
	v_exp_f32_e32 v107, v107
	v_exp_f32_e32 v108, v108
	s_waitcnt lgkmcnt(2)
	v_mfma_f32_32x32x64_f8f6f4 v[50:65], v[130:137], v[138:145], v[50:65]
	v_exp_f32_e32 v109, v109
	v_exp_f32_e32 v110, v110
	v_exp_f32_e32 v111, v111
	v_exp_f32_e32 v112, v112
	v_exp_f32_e32 v113, v113
	v_exp_f32_e32 v114, v114
	v_exp_f32_e32 v115, v115
	v_exp_f32_e32 v116, v116
	v_exp_f32_e32 v117, v117
	v_exp_f32_e32 v118, v118
	v_exp_f32_e32 v119, v119
	s_waitcnt lgkmcnt(0)
	v_mfma_f32_32x32x64_f8f6f4 v[66:81], v[130:137], v[162:169], v[66:81]
	v_exp_f32_e32 v120, v120
	v_exp_f32_e32 v121, v121
	v_exp_f32_e32 v122, v122
	v_exp_f32_e32 v123, v123
	v_exp_f32_e32 v124, v124
	v_exp_f32_e32 v125, v125
	v_exp_f32_e32 v126, v126
	v_exp_f32_e32 v127, v127
	v_exp_f32_e32 v128, v128
	v_exp_f32_e32 v129, v129
	s_andn2_b64 vcc, exec, s[38:39]
	s_cbranch_vccnz .LBB0_1326
	s_and_saveexec_b64 s[38:39], s[6:7]
	s_cbranch_execz .LBB0_1325
	ds_write_b32 v187, v170 offset:49152
	s_branch .LBB0_1325
.Lf_1326:
	v_cvt_pk_fp8_f32 v130, v98, v99
	v_cvt_pk_fp8_f32 v131, v102, v103
	ds_read_b128 v[138:141], v207 offset:0
	ds_read_b128 v[142:145], v209 offset:0
	ds_read_b128 v[162:165], v207 offset:0x800
	ds_read_b128 v[166:169], v209 offset:0x800
	v_cvt_pk_fp8_f32 v130, v100, v101 op_sel:[0,0,1]
	v_cvt_pk_fp8_f32 v131, v104, v105 op_sel:[0,0,1]
	s_waitcnt lgkmcnt(2)
	v_cvt_pk_fp8_f32 v132, v106, v107
	v_cvt_pk_fp8_f32 v133, v110, v111
	ds_read_b128 v[170:173], v188 offset:0
	ds_read_b128 v[174:177], v189 offset:0
	v_cvt_pk_fp8_f32 v132, v108, v109 op_sel:[0,0,1]
	v_cvt_pk_fp8_f32 v133, v112, v113 op_sel:[0,0,1]
	v_mfma_f32_32x32x64_f8f6f4 v[98:113], v[138:145], v[154:161], v[82:97]
	s_waitcnt lgkmcnt(2)
	v_cvt_pk_fp8_f32 v134, v114, v115
	v_cvt_pk_fp8_f32 v135, v118, v119
	v_cvt_pk_fp8_f32 v136, v122, v123
	v_cvt_pk_fp8_f32 v137, v126, v127
	v_cvt_pk_fp8_f32 v134, v116, v117 op_sel:[0,0,1]
	v_cvt_pk_fp8_f32 v135, v120, v121 op_sel:[0,0,1]
	v_cvt_pk_fp8_f32 v136, v124, v125 op_sel:[0,0,1]
	v_cvt_pk_fp8_f32 v137, v128, v129 op_sel:[0,0,1]
	v_mfma_f32_32x32x64_f8f6f4 v[114:129], v[162:169], v[154:161], v[82:97]
	ds_read_b128 v[138:141], v188 offset:0x800
	ds_read_b128 v[142:145], v189 offset:0x800
	s_nop 0
	v_mfma_f32_16x16x128_f8f6f4 v[18:21], v[130:137], v[146:153], v[18:21]
	s_waitcnt vmcnt(0) lgkmcnt(0)
	s_barrier
	s_add_i32 s37, s37, 4
	s_cmpk_lt_u32 s37, 0xfb
	s_cbranch_scc0 .LBB0_1354
.Lf_1327:
	s_waitcnt lgkmcnt(2)
	v_mfma_f32_32x32x64_f8f6f4 v[2:17], v[130:137], v[170:177], v[2:17]
	ds_read_b128 v[162:165], v188 offset:0x1000
	ds_read_b128 v[166:169], v189 offset:0x1000
.Lf_1330:
	s_waitcnt lgkmcnt(2)
	v_mfma_f32_32x32x64_f8f6f4 v[34:49], v[130:137], v[138:145], v[34:49]
	ds_read_b128 v[138:141], v188 offset:0x1800
	ds_read_b128 v[142:145], v189 offset:0x1800
	v_exp_f32_e32 v98, v98
	v_exp_f32_e32 v99, v99
	v_exp_f32_e32 v100, v100
	v_exp_f32_e32 v101, v101
	v_exp_f32_e32 v102, v102
	v_exp_f32_e32 v103, v103
	v_exp_f32_e32 v104, v104
	v_exp_f32_e32 v105, v105
	v_exp_f32_e32 v106, v106
	v_exp_f32_e32 v107, v107
	v_exp_f32_e32 v108, v108
	s_waitcnt lgkmcnt(2)
	v_mfma_f32_32x32x64_f8f6f4 v[50:65], v[130:137], v[162:169], v[50:65]
	v_exp_f32_e32 v109, v109
	v_exp_f32_e32 v110, v110
	v_exp_f32_e32 v111, v111
	v_exp_f32_e32 v112, v112
	v_exp_f32_e32 v113, v113
	v_exp_f32_e32 v114, v114
	v_exp_f32_e32 v115, v115
	v_exp_f32_e32 v116, v116
	v_exp_f32_e32 v117, v117
	v_exp_f32_e32 v118, v118
	v_exp_f32_e32 v119, v119
	s_waitcnt lgkmcnt(0)
	v_mfma_f32_32x32x64_f8f6f4 v[66:81], v[130:137], v[138:145], v[66:81]
	v_exp_f32_e32 v120, v120
	v_exp_f32_e32 v121, v121
	v_exp_f32_e32 v122, v122
	v_exp_f32_e32 v123, v123
	v_exp_f32_e32 v124, v124
	v_exp_f32_e32 v125, v125
	v_exp_f32_e32 v126, v126
	v_exp_f32_e32 v127, v127
	v_exp_f32_e32 v128, v128
	v_exp_f32_e32 v129, v129
.Lf_1334:
	v_cvt_pk_fp8_f32 v130, v98, v99
	v_cvt_pk_fp8_f32 v131, v102, v103
	ds_read_b128 v[138:141], v205 offset:0
	ds_read_b128 v[142:145], v206 offset:0
	ds_read_b128 v[170:173], v205 offset:0x800
	ds_read_b128 v[174:177], v206 offset:0x800
	v_cvt_pk_fp8_f32 v130, v100, v101 op_sel:[0,0,1]
	v_cvt_pk_fp8_f32 v131, v104, v105 op_sel:[0,0,1]
	s_waitcnt lgkmcnt(2)
	v_cvt_pk_fp8_f32 v132, v106, v107
	v_cvt_pk_fp8_f32 v133, v110, v111
	ds_read_b128 v[210:213], v203 offset:0
	ds_read_b128 v[214:217], v204 offset:0
	v_cvt_pk_fp8_f32 v132, v108, v109 op_sel:[0,0,1]
	v_cvt_pk_fp8_f32 v133, v112, v113 op_sel:[0,0,1]
	v_mfma_f32_32x32x64_f8f6f4 v[98:113], v[138:145], v[154:161], v[82:97]
	s_waitcnt lgkmcnt(2)
	v_cvt_pk_fp8_f32 v134, v114, v115
	v_cvt_pk_fp8_f32 v135, v118, v119
	v_cvt_pk_fp8_f32 v136, v122, v123
	v_cvt_pk_fp8_f32 v137, v126, v127
	v_cvt_pk_fp8_f32 v134, v116, v117 op_sel:[0,0,1]
	v_cvt_pk_fp8_f32 v135, v120, v121 op_sel:[0,0,1]
	v_cvt_pk_fp8_f32 v136, v124, v125 op_sel:[0,0,1]
	v_cvt_pk_fp8_f32 v137, v128, v129 op_sel:[0,0,1]
	v_mfma_f32_32x32x64_f8f6f4 v[114:129], v[170:177], v[154:161], v[82:97]
	ds_read_b128 v[162:165], v203 offset:0x800
	ds_read_b128 v[166:169], v204 offset:0x800
	s_nop 0
	v_mfma_f32_16x16x128_f8f6f4 v[18:21], v[130:137], v[146:153], v[18:21]
	s_waitcnt vmcnt(0) lgkmcnt(0)
	s_barrier
	s_waitcnt lgkmcnt(2)
	v_mfma_f32_32x32x64_f8f6f4 v[2:17], v[130:137], v[210:217], v[2:17]
	ds_read_b128 v[138:141], v203 offset:0x1000
	ds_read_b128 v[142:145], v204 offset:0x1000
.Lf_1337:
	s_waitcnt lgkmcnt(2)
	v_mfma_f32_32x32x64_f8f6f4 v[34:49], v[130:137], v[162:169], v[34:49]
	ds_read_b128 v[162:165], v203 offset:0x1800
	ds_read_b128 v[166:169], v204 offset:0x1800
	v_exp_f32_e32 v98, v98
	v_exp_f32_e32 v99, v99
	v_exp_f32_e32 v100, v100
	v_exp_f32_e32 v101, v101
	v_exp_f32_e32 v102, v102
	v_exp_f32_e32 v103, v103
	v_exp_f32_e32 v104, v104
	v_exp_f32_e32 v105, v105
	v_exp_f32_e32 v106, v106
	v_exp_f32_e32 v107, v107
	v_exp_f32_e32 v108, v108
	s_waitcnt lgkmcnt(2)
	v_mfma_f32_32x32x64_f8f6f4 v[50:65], v[130:137], v[138:145], v[50:65]
	v_exp_f32_e32 v109, v109
	v_exp_f32_e32 v110, v110
	v_exp_f32_e32 v111, v111
	v_exp_f32_e32 v112, v112
	v_exp_f32_e32 v113, v113
	v_exp_f32_e32 v114, v114
	v_exp_f32_e32 v115, v115
	v_exp_f32_e32 v116, v116
	v_exp_f32_e32 v117, v117
	v_exp_f32_e32 v118, v118
	v_exp_f32_e32 v119, v119
	s_waitcnt lgkmcnt(0)
	v_mfma_f32_32x32x64_f8f6f4 v[66:81], v[130:137], v[162:169], v[66:81]
	v_exp_f32_e32 v120, v120
	v_exp_f32_e32 v121, v121
	v_exp_f32_e32 v122, v122
	v_exp_f32_e32 v123, v123
	v_exp_f32_e32 v124, v124
	v_exp_f32_e32 v125, v125
	v_exp_f32_e32 v126, v126
	v_exp_f32_e32 v127, v127
	v_exp_f32_e32 v128, v128
	v_exp_f32_e32 v129, v129
.Lf_1341:
	v_cvt_pk_fp8_f32 v130, v98, v99
	v_cvt_pk_fp8_f32 v131, v102, v103
	ds_read_b128 v[138:141], v201 offset:0
	ds_read_b128 v[142:145], v202 offset:0
	ds_read_b128 v[170:173], v201 offset:0x800
	ds_read_b128 v[174:177], v202 offset:0x800
	v_cvt_pk_fp8_f32 v130, v100, v101 op_sel:[0,0,1]
	v_cvt_pk_fp8_f32 v131, v104, v105 op_sel:[0,0,1]
	s_waitcnt lgkmcnt(2)
	v_cvt_pk_fp8_f32 v132, v106, v107
	v_cvt_pk_fp8_f32 v133, v110, v111
	ds_read_b128 v[210:213], v199 offset:0
	ds_read_b128 v[214:217], v200 offset:0
	v_cvt_pk_fp8_f32 v132, v108, v109 op_sel:[0,0,1]
	v_cvt_pk_fp8_f32 v133, v112, v113 op_sel:[0,0,1]
	v_mfma_f32_32x32x64_f8f6f4 v[98:113], v[138:145], v[154:161], v[82:97]
	s_waitcnt lgkmcnt(2)
	v_cvt_pk_fp8_f32 v134, v114, v115
	v_cvt_pk_fp8_f32 v135, v118, v119
	v_cvt_pk_fp8_f32 v136, v122, v123
	v_cvt_pk_fp8_f32 v137, v126, v127
	v_cvt_pk_fp8_f32 v134, v116, v117 op_sel:[0,0,1]
	v_cvt_pk_fp8_f32 v135, v120, v121 op_sel:[0,0,1]
	v_cvt_pk_fp8_f32 v136, v124, v125 op_sel:[0,0,1]
	v_cvt_pk_fp8_f32 v137, v128, v129 op_sel:[0,0,1]
	v_mfma_f32_32x32x64_f8f6f4 v[114:129], v[170:177], v[154:161], v[82:97]
	ds_read_b128 v[162:165], v199 offset:0x800
	ds_read_b128 v[166:169], v200 offset:0x800
	s_nop 0
	v_mfma_f32_16x16x128_f8f6f4 v[18:21], v[130:137], v[146:153], v[18:21]
	s_waitcnt vmcnt(0) lgkmcnt(0)
	s_barrier
	s_waitcnt lgkmcnt(2)
	v_mfma_f32_32x32x64_f8f6f4 v[2:17], v[130:137], v[210:217], v[2:17]
	ds_read_b128 v[138:141], v199 offset:0x1000
	ds_read_b128 v[142:145], v200 offset:0x1000
.Lf_1344:
	s_waitcnt lgkmcnt(2)
	v_mfma_f32_32x32x64_f8f6f4 v[34:49], v[130:137], v[162:169], v[34:49]
	ds_read_b128 v[162:165], v199 offset:0x1800
	ds_read_b128 v[166:169], v200 offset:0x1800
	v_exp_f32_e32 v98, v98
	v_exp_f32_e32 v99, v99
	v_exp_f32_e32 v100, v100
	v_exp_f32_e32 v101, v101
	v_exp_f32_e32 v102, v102
	v_exp_f32_e32 v103, v103
	v_exp_f32_e32 v104, v104
	v_exp_f32_e32 v105, v105
	v_exp_f32_e32 v106, v106
	v_exp_f32_e32 v107, v107
	v_exp_f32_e32 v108, v108
	s_waitcnt lgkmcnt(2)
	v_mfma_f32_32x32x64_f8f6f4 v[50:65], v[130:137], v[138:145], v[50:65]
	v_exp_f32_e32 v109, v109
	v_exp_f32_e32 v110, v110
	v_exp_f32_e32 v111, v111
	v_exp_f32_e32 v112, v112
	v_exp_f32_e32 v113, v113
	v_exp_f32_e32 v114, v114
	v_exp_f32_e32 v115, v115
	v_exp_f32_e32 v116, v116
	v_exp_f32_e32 v117, v117
	v_exp_f32_e32 v118, v118
	v_exp_f32_e32 v119, v119
	s_waitcnt lgkmcnt(0)
	v_mfma_f32_32x32x64_f8f6f4 v[66:81], v[130:137], v[162:169], v[66:81]
	v_exp_f32_e32 v120, v120
	v_exp_f32_e32 v121, v121
	v_exp_f32_e32 v122, v122
	v_exp_f32_e32 v123, v123
	v_exp_f32_e32 v124, v124
	v_exp_f32_e32 v125, v125
	v_exp_f32_e32 v126, v126
	v_exp_f32_e32 v127, v127
	v_exp_f32_e32 v128, v128
	v_exp_f32_e32 v129, v129
.Lf_1348:
	v_cvt_pk_fp8_f32 v130, v98, v99
	v_cvt_pk_fp8_f32 v131, v102, v103
	ds_read_b128 v[138:141], v183 offset:0
	ds_read_b128 v[142:145], v190 offset:0
	ds_read_b128 v[170:173], v183 offset:0x800
	ds_read_b128 v[174:177], v190 offset:0x800
	v_cvt_pk_fp8_f32 v130, v100, v101 op_sel:[0,0,1]
	v_cvt_pk_fp8_f32 v131, v104, v105 op_sel:[0,0,1]
	s_waitcnt lgkmcnt(2)
	v_cvt_pk_fp8_f32 v132, v106, v107
	v_cvt_pk_fp8_f32 v133, v110, v111
	ds_read_b128 v[210:213], v196 offset:0
	ds_read_b128 v[214:217], v197 offset:0
	v_cvt_pk_fp8_f32 v132, v108, v109 op_sel:[0,0,1]
	v_cvt_pk_fp8_f32 v133, v112, v113 op_sel:[0,0,1]
	v_mfma_f32_32x32x64_f8f6f4 v[98:113], v[138:145], v[154:161], v[82:97]
	s_waitcnt lgkmcnt(2)
	v_cvt_pk_fp8_f32 v134, v114, v115
	v_cvt_pk_fp8_f32 v135, v118, v119
	v_cvt_pk_fp8_f32 v136, v122, v123
	v_cvt_pk_fp8_f32 v137, v126, v127
	v_cvt_pk_fp8_f32 v134, v116, v117 op_sel:[0,0,1]
	v_cvt_pk_fp8_f32 v135, v120, v121 op_sel:[0,0,1]
	v_cvt_pk_fp8_f32 v136, v124, v125 op_sel:[0,0,1]
	v_cvt_pk_fp8_f32 v137, v128, v129 op_sel:[0,0,1]
	v_mfma_f32_32x32x64_f8f6f4 v[114:129], v[170:177], v[154:161], v[82:97]
	ds_read_b128 v[162:165], v196 offset:0x800
	ds_read_b128 v[166:169], v197 offset:0x800
	s_nop 0
	v_mfma_f32_16x16x128_f8f6f4 v[18:21], v[130:137], v[146:153], v[18:21]
	s_waitcnt vmcnt(0) lgkmcnt(0)
	s_barrier
	s_waitcnt lgkmcnt(2)
	v_mfma_f32_32x32x64_f8f6f4 v[2:17], v[130:137], v[210:217], v[2:17]
	ds_read_b128 v[138:141], v196 offset:0x1000
	ds_read_b128 v[142:145], v197 offset:0x1000

.LBB0_1376:
	s_and_b64 vcc, exec, s[38:39]
	s_cbranch_vccz .LBB0_1202
	ds_read_b128 v[18:21], v183 offset:0
	ds_read_b128 v[22:25], v190 offset:0
	ds_read_b128 v[34:37], v183 offset:0x800
	ds_read_b128 v[38:41], v190 offset:0x800
	s_waitcnt lgkmcnt(0)
	s_waitcnt vmcnt(0)
	s_nop 11
	v_mfma_f32_32x32x64_f8f6f4 v[18:33], v[18:25], v[154:161], 0
	s_mov_b32 s37, s36
	s_mov_b32 s38, s36
	s_mov_b32 s39, s36
	s_mov_b32 s40, s36
	s_mov_b32 s41, s36
	s_mov_b32 s42, s36
	s_mov_b32 s43, s36
	s_mov_b32 s44, s36
	s_mov_b32 s45, s36
	s_mov_b32 s46, s36
	s_mov_b32 s47, s36
	s_mov_b32 s48, s36
	s_mov_b32 s49, s36
	s_mov_b32 s50, s36
	s_mov_b32 s51, s36
	v_mov_b64_e32 v[2:3], s[36:37]
	v_mov_b64_e32 v[4:5], s[38:39]
	v_mov_b64_e32 v[6:7], s[40:41]
	v_mov_b64_e32 v[8:9], s[42:43]
	v_mov_b64_e32 v[10:11], s[44:45]
	v_mov_b64_e32 v[12:13], s[46:47]
	v_mov_b64_e32 v[14:15], s[48:49]
	v_mov_b64_e32 v[16:17], s[50:51]
	v_max_f32_e32 v42, v19, v19
	v_max_f32_e32 v43, v18, v18
	v_max_f32_e32 v42, v43, v42
	v_max3_f32 v42, v42, v20, v21
	v_max3_f32 v42, v42, v22, v23
	v_max3_f32 v42, v42, v24, v25
	v_max3_f32 v42, v42, v26, v27
	v_max3_f32 v42, v42, v28, v29
	v_max3_f32 v50, v42, v30, v31
	v_mfma_f32_32x32x64_f8f6f4 v[34:49], v[34:41], v[154:161], 0
	v_max3_f32 v50, v50, v32, v33
	s_lshl_b32 s45, s95, 10
	s_lshl_b32 s46, s81, 10
	s_cmp_lg_u32 0, -1
	s_cselect_b32 s38, 0, 0
	s_add_i32 s37, s38, 0x2000
	s_add_i32 s39, s38, 0x3000
	s_add_i32 s6, s38, 0x1000
	v_add_u32_e32 v203, s37, v194
	s_add_i32 s37, s38, 0x6000
	v_add_u32_e32 v199, s39, v194
	s_add_i32 s39, s38, 0x8000
	s_add_i32 s38, s38, 0xa000
	v_add_u32_e32 v205, s6, v194
	v_add_u32_e32 v201, s37, v194
	s_nop 4
	v_max3_f32 v50, v50, v34, v35
	v_max3_f32 v50, v50, v36, v37
	v_max3_f32 v50, v50, v38, v39
	v_max3_f32 v50, v50, v40, v41
	v_max3_f32 v50, v50, v42, v43
	v_max3_f32 v50, v50, v44, v45
	v_max3_f32 v50, v50, v46, v47
	v_max3_f32 v50, v50, v48, v49
	v_mov_b32_e32 v51, v50
	s_nop 1
	v_permlane32_swap_b32_e32 v50, v51
	v_max_f32_e32 v51, v51, v51
	v_max_f32_e32 v50, v50, v50
	v_max_f32_e32 v50, v50, v51
	s_cmp_eq_u32 s98, 0
	s_cselect_b32 s100, 0x40000000, 0xc0600000
	v_add_f32_e32 v198, s100, v50
	v_sub_f32_e32 v18, v18, v198
	v_sub_f32_e32 v19, v19, v198
	v_add_u32_e32 v196, s39, v194
	v_add_u32_e32 v194, s38, v194
	s_lshl_b32 s38, s80, 4
	v_exp_f32_e32 v114, v18
	v_exp_f32_e32 v115, v19
	v_lshl_add_u64 v[18:19], s[16:17], 0, v[180:181]
	s_and_b32 s38, s38, 0xfffffc00
	s_ashr_i32 s89, s88, 31
	s_or_b32 s40, s88, 0x100
	s_add_i32 s41, s94, 0x4100
	s_or_b32 s42, s88, 0x140
	s_add_i32 s43, s94, 0x4140
	v_lshl_add_u64 v[170:171], v[18:19], 0, s[28:29]
	v_lshl_or_b32 v18, v193, 4, s38
	s_lshl_b64 s[38:39], s[88:89], 10
	s_add_u32 s38, s38, s87
	v_xor_b32_e32 v82, 0x80000000, v198
	v_sub_f32_e32 v34, v34, v198
	v_sub_f32_e32 v35, v35, v198
	v_sub_f32_e32 v20, v20, v198
	v_sub_f32_e32 v36, v36, v198
	v_sub_f32_e32 v21, v21, v198
	v_sub_f32_e32 v37, v37, v198
	v_sub_f32_e32 v22, v22, v198
	v_sub_f32_e32 v38, v38, v198
	v_sub_f32_e32 v23, v23, v198
	v_sub_f32_e32 v39, v39, v198
	v_sub_f32_e32 v24, v24, v198
	v_sub_f32_e32 v40, v40, v198
	v_sub_f32_e32 v25, v25, v198
	v_sub_f32_e32 v41, v41, v198
	v_sub_f32_e32 v26, v26, v198
	v_sub_f32_e32 v42, v42, v198
	v_sub_f32_e32 v27, v27, v198
	v_sub_f32_e32 v43, v43, v198
	v_sub_f32_e32 v28, v28, v198
	v_sub_f32_e32 v44, v44, v198
	v_sub_f32_e32 v29, v29, v198
	v_sub_f32_e32 v45, v45, v198
	v_sub_f32_e32 v30, v30, v198
	v_sub_f32_e32 v46, v46, v198
	v_sub_f32_e32 v31, v31, v198
	v_sub_f32_e32 v47, v47, v198
	v_sub_f32_e32 v32, v32, v198
	v_sub_f32_e32 v48, v48, v198
	v_sub_f32_e32 v33, v33, v198
	v_sub_f32_e32 v49, v49, v198
	s_addc_u32 s39, s39, s76
	v_mov_b32_e32 v83, v82
	v_mov_b32_e32 v84, v82
	v_mov_b32_e32 v85, v82
	v_mov_b32_e32 v86, v82
	v_mov_b32_e32 v87, v82
	v_mov_b32_e32 v88, v82
	v_mov_b32_e32 v89, v82
	v_mov_b32_e32 v90, v82
	v_mov_b32_e32 v91, v82
	v_mov_b32_e32 v92, v82
	v_mov_b32_e32 v93, v82
	v_mov_b32_e32 v94, v82
	v_mov_b32_e32 v95, v82
	v_mov_b32_e32 v96, v82
	v_mov_b32_e32 v97, v82
	v_exp_f32_e32 v98, v34
	v_exp_f32_e32 v99, v35
	v_exp_f32_e32 v116, v20
	v_exp_f32_e32 v100, v36
	v_exp_f32_e32 v117, v21
	v_exp_f32_e32 v101, v37
	v_exp_f32_e32 v118, v22
	v_exp_f32_e32 v102, v38
	v_exp_f32_e32 v119, v23
	v_exp_f32_e32 v103, v39
	v_exp_f32_e32 v120, v24
	v_exp_f32_e32 v104, v40
	v_exp_f32_e32 v121, v25
	v_exp_f32_e32 v105, v41
	v_exp_f32_e32 v122, v26
	v_exp_f32_e32 v106, v42
	v_exp_f32_e32 v123, v27
	v_exp_f32_e32 v107, v43
	v_exp_f32_e32 v124, v28
	v_exp_f32_e32 v108, v44
	v_exp_f32_e32 v125, v29
	v_exp_f32_e32 v109, v45
	v_exp_f32_e32 v126, v30
	v_exp_f32_e32 v110, v46
	v_exp_f32_e32 v127, v31
	v_exp_f32_e32 v111, v47
	v_exp_f32_e32 v128, v32
	v_exp_f32_e32 v112, v48
	v_exp_f32_e32 v129, v33
	v_exp_f32_e32 v113, v49
	v_mov_b32_e32 v19, v181
	s_add_u32 s38, s38, 0x29c30040
	s_waitcnt vmcnt(3) lgkmcnt(0)
	s_barrier
	v_lshl_add_u64 v[172:173], s[92:93], 0, v[18:19]
	s_addc_u32 s39, s39, 0
	v_add3_u32 v18, s79, v191, v192
	v_lshl_add_u64 v[174:175], s[38:39], 0, v[18:19]
	v_mov_b32_e32 v162, 0
	v_mov_b64_e32 v[48:49], v[16:17]
	v_mov_b64_e32 v[64:65], v[16:17]
	v_mov_b64_e32 v[80:81], v[16:17]
	v_mov_b64_e32 v[32:33], v[16:17]
	v_add_u32_e32 v206, v205, v195
	v_cmp_gt_u32_e64 s[6:7], 32, v193
	v_add_u32_e32 v204, v203, v195
	v_add_u32_e32 v202, v201, v195
	s_movk_i32 s37, 0x100
	v_add_u32_e32 v200, v199, v195
	v_add_u32_e32 v197, v196, v195
	v_add_u32_e32 v195, v194, v195
	s_mov_b32 s44, -3
	s_add_i32 s45, s45, 0
	s_add_i32 s46, s46, 0
	v_mov_b64_e32 v[46:47], v[14:15]
	v_mov_b64_e32 v[44:45], v[12:13]
	v_mov_b64_e32 v[42:43], v[10:11]
	v_mov_b64_e32 v[40:41], v[8:9]
	v_mov_b64_e32 v[38:39], v[6:7]
	v_mov_b64_e32 v[36:37], v[4:5]
	v_mov_b64_e32 v[34:35], v[2:3]
	v_mov_b64_e32 v[62:63], v[14:15]
	v_mov_b64_e32 v[60:61], v[12:13]
	v_mov_b64_e32 v[58:59], v[10:11]
	v_mov_b64_e32 v[56:57], v[8:9]
	v_mov_b64_e32 v[54:55], v[6:7]
	v_mov_b64_e32 v[52:53], v[4:5]
	v_mov_b64_e32 v[50:51], v[2:3]
	v_mov_b64_e32 v[78:79], v[14:15]
	v_mov_b64_e32 v[76:77], v[12:13]
	v_mov_b64_e32 v[74:75], v[10:11]
	v_mov_b64_e32 v[72:73], v[8:9]
	v_mov_b64_e32 v[70:71], v[6:7]
	v_mov_b64_e32 v[68:69], v[4:5]
	v_mov_b64_e32 v[66:67], v[2:3]
	v_mov_b64_e32 v[30:31], v[14:15]
	v_mov_b64_e32 v[28:29], v[12:13]
	v_mov_b64_e32 v[26:27], v[10:11]
	v_mov_b64_e32 v[24:25], v[8:9]
	v_mov_b64_e32 v[22:23], v[6:7]
	v_mov_b64_e32 v[20:21], v[4:5]
	v_mov_b64_e32 v[18:19], v[2:3]
	v_mov_b32_e32 v163, v162
	v_mov_b32_e32 v164, v162
	v_mov_b32_e32 v165, v162
	v_mov_b32_e32 v166, v162
	v_mov_b32_e32 v167, v162
	v_mov_b32_e32 v168, v162
	v_mov_b32_e32 v169, v162
	s_cmp_lg_u32 s98, 0
	s_cbranch_scc1 .LBB0_1380
	s_branch .Lf_1380

.LBB0_1404:
	s_waitcnt lgkmcnt(2)
	v_mfma_f32_32x32x64_f8f6f4 v[34:49], v[162:169], v[138:145], v[34:49]
	ds_read_b128 v[138:141], v194 offset:0x1800
	ds_read_b128 v[142:145], v195 offset:0x1800
	v_exp_f32_e32 v114, v114
	v_exp_f32_e32 v115, v115
	v_exp_f32_e32 v116, v116
	v_exp_f32_e32 v117, v117
	v_exp_f32_e32 v118, v118
	v_exp_f32_e32 v119, v119
	v_exp_f32_e32 v120, v120
	v_exp_f32_e32 v121, v121
	v_exp_f32_e32 v122, v122
	v_exp_f32_e32 v123, v123
	v_exp_f32_e32 v124, v124
	s_waitcnt lgkmcnt(2)
	v_mfma_f32_32x32x64_f8f6f4 v[50:65], v[162:169], v[130:137], v[50:65]
	v_exp_f32_e32 v125, v125
	v_exp_f32_e32 v126, v126
	v_exp_f32_e32 v127, v127
	v_exp_f32_e32 v128, v128
	v_exp_f32_e32 v129, v129
	v_exp_f32_e32 v98, v98
	v_exp_f32_e32 v99, v99
	v_exp_f32_e32 v100, v100
	v_exp_f32_e32 v101, v101
	v_exp_f32_e32 v102, v102
	v_exp_f32_e32 v103, v103
	s_waitcnt lgkmcnt(0)
	v_mfma_f32_32x32x64_f8f6f4 v[66:81], v[162:169], v[138:145], v[66:81]
	v_exp_f32_e32 v104, v104
	v_exp_f32_e32 v105, v105
	v_exp_f32_e32 v106, v106
	v_exp_f32_e32 v107, v107
	v_exp_f32_e32 v108, v108
	v_exp_f32_e32 v109, v109
	v_exp_f32_e32 v110, v110
	v_exp_f32_e32 v111, v111
	v_exp_f32_e32 v112, v112
	v_exp_f32_e32 v113, v113
	s_andn2_b64 vcc, exec, s[38:39]
	s_cbranch_vccnz .LBB0_1379
	s_and_saveexec_b64 s[38:39], s[6:7]
	s_cbranch_execz .LBB0_1378
	ds_write_b32 v187, v176 offset:49152
	s_branch .LBB0_1378
.Lf_1379:
	s_waitcnt vmcnt(3) lgkmcnt(0)
	s_barrier
	s_addk_i32 s37, 0x100
	v_lshl_add_u64 v[172:173], v[172:173], 0, s[72:73]
	s_cmpk_lt_u32 s44, 0xfa
	v_lshl_add_u64 v[174:175], v[174:175], 0, s[74:75]
	s_cbranch_scc0 .LBB0_1407
.Lf_1380:
	s_add_i32 s49, s45, 0x3000
	v_lshl_add_u64 v[130:131], s[14:15], 0, v[174:175]
	s_mov_b32 m0, s49
	v_lshl_add_u64 v[176:177], s[14:15], 0, v[172:173]
	s_add_i32 s47, s46, 0x8000
	global_load_lds_dwordx4 v[130:131], off
	v_lshl_add_u64 v[130:131], v[176:177], 0, s[56:57]
	s_mov_b32 m0, s47
	s_add_i32 s48, s46, 0x9000
	global_load_lds_dwordx4 v[130:131], off
	v_lshl_add_u64 v[130:131], v[176:177], 0, s[58:59]
	s_mov_b32 m0, s48
	v_cvt_pk_fp8_f32 v162, v114, v115
	global_load_lds_dwordx4 v[130:131], off
	v_cvt_pk_fp8_f32 v163, v118, v119
	ds_read_b128 v[130:133], v205 offset:0
	ds_read_b128 v[134:137], v206 offset:0
	ds_read_b128 v[210:213], v205 offset:0x800
	ds_read_b128 v[214:217], v206 offset:0x800
	v_cvt_pk_fp8_f32 v162, v116, v117 op_sel:[0,0,1]
	v_cvt_pk_fp8_f32 v163, v120, v121 op_sel:[0,0,1]
	s_waitcnt lgkmcnt(2)
	v_cvt_pk_fp8_f32 v164, v122, v123
	v_cvt_pk_fp8_f32 v165, v126, v127
	ds_read_b128 v[218:221], v188 offset:0
	ds_read_b128 v[222:225], v189 offset:0
	v_cvt_pk_fp8_f32 v164, v124, v125 op_sel:[0,0,1]
	v_cvt_pk_fp8_f32 v165, v128, v129 op_sel:[0,0,1]
	v_mfma_f32_32x32x64_f8f6f4 v[114:129], v[130:137], v[154:161], v[82:97]
	s_waitcnt lgkmcnt(2)
	v_mfma_f32_32x32x64_f8f6f4 v[130:145], v[210:217], v[154:161], v[82:97]
	v_cvt_pk_fp8_f32 v166, v98, v99
	v_cvt_pk_fp8_f32 v167, v102, v103
	v_cvt_pk_fp8_f32 v168, v106, v107
	v_cvt_pk_fp8_f32 v169, v110, v111
	v_cvt_pk_fp8_f32 v166, v100, v101 op_sel:[0,0,1]
	v_cvt_pk_fp8_f32 v167, v104, v105 op_sel:[0,0,1]
	v_cvt_pk_fp8_f32 v168, v108, v109 op_sel:[0,0,1]
	v_cvt_pk_fp8_f32 v169, v112, v113 op_sel:[0,0,1]
	s_nop 0
	ds_read_b128 v[106:109], v188 offset:0x800
	ds_read_b128 v[110:113], v189 offset:0x800
	s_nop 0
	v_mfma_f32_16x16x128_f8f6f4 v[18:21], v[162:169], v[146:153], v[18:21]
	s_waitcnt lgkmcnt(2)
	v_mfma_f32_32x32x64_f8f6f4 v[2:17], v[162:169], v[218:225], v[2:17]
	ds_read_b128 v[98:101], v188 offset:0x1000
	ds_read_b128 v[102:105], v189 offset:0x1000
.Lf_1383:
	s_waitcnt lgkmcnt(2)
	v_mfma_f32_32x32x64_f8f6f4 v[34:49], v[162:169], v[106:113], v[34:49]
	ds_read_b128 v[106:109], v188 offset:0x1800
	ds_read_b128 v[110:113], v189 offset:0x1800
	v_exp_f32_e32 v114, v114
	v_exp_f32_e32 v115, v115
	v_exp_f32_e32 v116, v116
	v_exp_f32_e32 v117, v117
	v_exp_f32_e32 v118, v118
	v_exp_f32_e32 v119, v119
	v_exp_f32_e32 v120, v120
	v_exp_f32_e32 v121, v121
	v_exp_f32_e32 v122, v122
	v_exp_f32_e32 v123, v123
	v_exp_f32_e32 v124, v124
	s_waitcnt lgkmcnt(2)
	v_mfma_f32_32x32x64_f8f6f4 v[50:65], v[162:169], v[98:105], v[50:65]
	v_exp_f32_e32 v125, v125
	v_exp_f32_e32 v126, v126
	v_exp_f32_e32 v127, v127
	v_exp_f32_e32 v128, v128
	v_exp_f32_e32 v129, v129
	v_exp_f32_e32 v130, v130
	v_exp_f32_e32 v131, v131
	v_exp_f32_e32 v132, v132
	v_exp_f32_e32 v133, v133
	v_exp_f32_e32 v134, v134
	v_exp_f32_e32 v135, v135
	s_waitcnt lgkmcnt(0)
	v_mfma_f32_32x32x64_f8f6f4 v[66:81], v[162:169], v[106:113], v[66:81]
	v_exp_f32_e32 v136, v136
	v_exp_f32_e32 v137, v137
	v_exp_f32_e32 v138, v138
	v_exp_f32_e32 v139, v139
	v_exp_f32_e32 v140, v140
	v_exp_f32_e32 v141, v141
	v_exp_f32_e32 v142, v142
	v_exp_f32_e32 v143, v143
	v_exp_f32_e32 v144, v144
	v_exp_f32_e32 v145, v145
.Lf_1387:
	s_add_i32 s38, s88, s37
	s_cmpk_eq_i32 s44, 0xf9
	s_cselect_b32 s38, s77, s38
	s_ashr_i32 s39, s38, 31
	s_lshl_b64 s[38:39], s[38:39], 10
	s_mov_b32 m0, s45
	s_waitcnt vmcnt(3) lgkmcnt(0)
	s_barrier
	v_lshl_add_u64 v[98:99], v[170:171], 0, s[38:39]
	s_add_i32 s51, s46, 0xa000
	global_load_lds_dwordx4 v[98:99], off
	v_lshl_add_u64 v[98:99], v[176:177], 0, s[60:61]
	s_mov_b32 m0, s51
	s_add_i32 s50, s46, 0xb000
	global_load_lds_dwordx4 v[98:99], off
	v_lshl_add_u64 v[98:99], v[176:177], 0, s[62:63]
	s_mov_b32 m0, s50
	v_cvt_pk_fp8_f32 v162, v114, v115
	global_load_lds_dwordx4 v[98:99], off
	v_cvt_pk_fp8_f32 v163, v118, v119
	ds_read_b128 v[210:213], v203 offset:0
	ds_read_b128 v[214:217], v204 offset:0
	ds_read_b128 v[218:221], v203 offset:0x800
	ds_read_b128 v[222:225], v204 offset:0x800
	v_cvt_pk_fp8_f32 v162, v116, v117 op_sel:[0,0,1]
	v_cvt_pk_fp8_f32 v163, v120, v121 op_sel:[0,0,1]
	s_waitcnt lgkmcnt(2)
	v_mfma_f32_32x32x64_f8f6f4 v[98:113], v[210:217], v[154:161], v[82:97]
	v_cvt_pk_fp8_f32 v164, v122, v123
	v_cvt_pk_fp8_f32 v165, v126, v127
	ds_read_b128 v[226:229], v201 offset:0
	ds_read_b128 v[230:233], v202 offset:0
	v_cvt_pk_fp8_f32 v164, v124, v125 op_sel:[0,0,1]
	v_cvt_pk_fp8_f32 v165, v128, v129 op_sel:[0,0,1]
	s_waitcnt lgkmcnt(2)
	v_mfma_f32_32x32x64_f8f6f4 v[114:129], v[218:225], v[154:161], v[82:97]
	v_cvt_pk_fp8_f32 v166, v130, v131
	v_cvt_pk_fp8_f32 v167, v134, v135
	v_cvt_pk_fp8_f32 v168, v138, v139
	v_cvt_pk_fp8_f32 v169, v142, v143
	v_cvt_pk_fp8_f32 v166, v132, v133 op_sel:[0,0,1]
	v_cvt_pk_fp8_f32 v167, v136, v137 op_sel:[0,0,1]
	v_cvt_pk_fp8_f32 v168, v140, v141 op_sel:[0,0,1]
	v_cvt_pk_fp8_f32 v169, v144, v145 op_sel:[0,0,1]
	s_nop 0
	ds_read_b128 v[138:141], v201 offset:0x800
	ds_read_b128 v[142:145], v202 offset:0x800
	s_nop 0
	v_mfma_f32_16x16x128_f8f6f4 v[18:21], v[162:169], v[146:153], v[18:21]
	s_waitcnt lgkmcnt(2)
	v_mfma_f32_32x32x64_f8f6f4 v[2:17], v[162:169], v[226:233], v[2:17]
	ds_read_b128 v[130:133], v201 offset:0x1000
	ds_read_b128 v[134:137], v202 offset:0x1000
.Lf_1390:
	s_waitcnt lgkmcnt(2)
	v_mfma_f32_32x32x64_f8f6f4 v[34:49], v[162:169], v[138:145], v[34:49]
	ds_read_b128 v[138:141], v201 offset:0x1800
	ds_read_b128 v[142:145], v202 offset:0x1800
	v_exp_f32_e32 v98, v98
	v_exp_f32_e32 v99, v99
	v_exp_f32_e32 v100, v100
	v_exp_f32_e32 v101, v101
	v_exp_f32_e32 v102, v102
	v_exp_f32_e32 v103, v103
	v_exp_f32_e32 v104, v104
	v_exp_f32_e32 v105, v105
	v_exp_f32_e32 v106, v106
	v_exp_f32_e32 v107, v107
	v_exp_f32_e32 v108, v108
	s_waitcnt lgkmcnt(2)
	v_mfma_f32_32x32x64_f8f6f4 v[50:65], v[162:169], v[130:137], v[50:65]
	v_exp_f32_e32 v109, v109
	v_exp_f32_e32 v110, v110
	v_exp_f32_e32 v111, v111
	v_exp_f32_e32 v112, v112
	v_exp_f32_e32 v113, v113
	v_exp_f32_e32 v114, v114
	v_exp_f32_e32 v115, v115
	v_exp_f32_e32 v116, v116
	v_exp_f32_e32 v117, v117
	v_exp_f32_e32 v118, v118
	v_exp_f32_e32 v119, v119
	s_waitcnt lgkmcnt(0)
	v_mfma_f32_32x32x64_f8f6f4 v[66:81], v[162:169], v[138:145], v[66:81]
	v_exp_f32_e32 v120, v120
	v_exp_f32_e32 v121, v121
	v_exp_f32_e32 v122, v122
	v_exp_f32_e32 v123, v123
	v_exp_f32_e32 v124, v124
	v_exp_f32_e32 v125, v125
	v_exp_f32_e32 v126, v126
	v_exp_f32_e32 v127, v127
	v_exp_f32_e32 v128, v128
	v_exp_f32_e32 v129, v129
.Lf_1394:
	s_add_i32 s44, s44, 4
	s_cmpk_lt_u32 s44, 0xfc
	s_cselect_b32 s38, s40, s41
	s_add_i32 s38, s38, s37
	s_addk_i32 s38, 0xff40
	s_ashr_i32 s39, s38, 31
	s_lshl_b64 s[38:39], s[38:39], 10
	s_waitcnt vmcnt(3) lgkmcnt(0)
	s_barrier
	v_lshl_add_u64 v[130:131], v[170:171], 0, s[38:39]
	s_add_i32 m0, s45, 0x1000
	v_cvt_pk_fp8_f32 v162, v98, v99
	global_load_lds_dwordx4 v[130:131], off
	v_lshl_add_u64 v[130:131], v[176:177], 0, s[64:65]
	s_add_i32 m0, s46, 0x4000
	v_cvt_pk_fp8_f32 v163, v102, v103
	global_load_lds_dwordx4 v[130:131], off
	v_lshl_add_u64 v[130:131], v[176:177], 0, s[66:67]
	s_add_i32 m0, s46, 0x5000
	v_cvt_pk_fp8_f32 v162, v100, v101 op_sel:[0,0,1]
	global_load_lds_dwordx4 v[130:131], off
	ds_read_b128 v[130:133], v199 offset:0
	ds_read_b128 v[134:137], v200 offset:0
	ds_read_b128 v[210:213], v199 offset:0x800
	ds_read_b128 v[214:217], v200 offset:0x800
	v_cvt_pk_fp8_f32 v163, v104, v105 op_sel:[0,0,1]
	s_waitcnt lgkmcnt(2)
	v_cvt_pk_fp8_f32 v164, v106, v107
	v_cvt_pk_fp8_f32 v165, v110, v111
	ds_read_b128 v[218:221], v196 offset:0
	ds_read_b128 v[222:225], v197 offset:0
	v_cvt_pk_fp8_f32 v164, v108, v109 op_sel:[0,0,1]
	v_cvt_pk_fp8_f32 v165, v112, v113 op_sel:[0,0,1]
	v_mfma_f32_32x32x64_f8f6f4 v[98:113], v[130:137], v[154:161], v[82:97]
	s_waitcnt lgkmcnt(2)
	v_mfma_f32_32x32x64_f8f6f4 v[130:145], v[210:217], v[154:161], v[82:97]
	v_cvt_pk_fp8_f32 v166, v114, v115
	v_cvt_pk_fp8_f32 v167, v118, v119
	v_cvt_pk_fp8_f32 v168, v122, v123
	v_cvt_pk_fp8_f32 v169, v126, v127
	v_cvt_pk_fp8_f32 v166, v116, v117 op_sel:[0,0,1]
	v_cvt_pk_fp8_f32 v167, v120, v121 op_sel:[0,0,1]
	v_cvt_pk_fp8_f32 v168, v124, v125 op_sel:[0,0,1]
	v_cvt_pk_fp8_f32 v169, v128, v129 op_sel:[0,0,1]
	s_nop 0
	ds_read_b128 v[122:125], v196 offset:0x800
	ds_read_b128 v[126:129], v197 offset:0x800
	s_nop 0
	v_mfma_f32_16x16x128_f8f6f4 v[18:21], v[162:169], v[146:153], v[18:21]
	s_waitcnt lgkmcnt(2)
	v_mfma_f32_32x32x64_f8f6f4 v[2:17], v[162:169], v[218:225], v[2:17]
	ds_read_b128 v[114:117], v196 offset:0x1000
	ds_read_b128 v[118:121], v197 offset:0x1000
.Lf_1397:
	s_waitcnt lgkmcnt(2)
	v_mfma_f32_32x32x64_f8f6f4 v[34:49], v[162:169], v[122:129], v[34:49]
	ds_read_b128 v[122:125], v196 offset:0x1800
	ds_read_b128 v[126:129], v197 offset:0x1800
	v_exp_f32_e32 v98, v98
	v_exp_f32_e32 v99, v99
	v_exp_f32_e32 v100, v100
	v_exp_f32_e32 v101, v101
	v_exp_f32_e32 v102, v102
	v_exp_f32_e32 v103, v103
	v_exp_f32_e32 v104, v104
	v_exp_f32_e32 v105, v105
	v_exp_f32_e32 v106, v106
	v_exp_f32_e32 v107, v107
	v_exp_f32_e32 v108, v108
	s_waitcnt lgkmcnt(2)
	v_mfma_f32_32x32x64_f8f6f4 v[50:65], v[162:169], v[114:121], v[50:65]
	v_exp_f32_e32 v109, v109
	v_exp_f32_e32 v110, v110
	v_exp_f32_e32 v111, v111
	v_exp_f32_e32 v112, v112
	v_exp_f32_e32 v113, v113
	v_exp_f32_e32 v130, v130
	v_exp_f32_e32 v131, v131
	v_exp_f32_e32 v132, v132
	v_exp_f32_e32 v133, v133
	v_exp_f32_e32 v134, v134
	v_exp_f32_e32 v135, v135
	s_waitcnt lgkmcnt(0)
	v_mfma_f32_32x32x64_f8f6f4 v[66:81], v[162:169], v[122:129], v[66:81]
	v_exp_f32_e32 v136, v136
	v_exp_f32_e32 v137, v137
	v_exp_f32_e32 v138, v138
	v_exp_f32_e32 v139, v139
	v_exp_f32_e32 v140, v140
	v_exp_f32_e32 v141, v141
	v_exp_f32_e32 v142, v142
	v_exp_f32_e32 v143, v143
	v_exp_f32_e32 v144, v144
	v_exp_f32_e32 v145, v145
.Lf_1401:
	s_cmpk_lt_u32 s44, 0xfb
	s_cselect_b32 s38, s42, s43
	s_add_i32 s38, s38, s37
	s_addk_i32 s38, 0xff40
	s_ashr_i32 s39, s38, 31
	s_lshl_b64 s[38:39], s[38:39], 10
	s_waitcnt vmcnt(3) lgkmcnt(0)
	s_barrier
	v_lshl_add_u64 v[114:115], v[170:171], 0, s[38:39]
	s_add_i32 m0, s45, 0x2000
	v_cvt_pk_fp8_f32 v162, v98, v99
	global_load_lds_dwordx4 v[114:115], off
	v_lshl_add_u64 v[114:115], v[176:177], 0, s[68:69]
	s_add_i32 m0, s46, 0x6000
	v_cvt_pk_fp8_f32 v163, v102, v103
	global_load_lds_dwordx4 v[114:115], off
	v_lshl_add_u64 v[114:115], v[176:177], 0, s[70:71]
	s_add_i32 m0, s46, 0x7000
	v_cvt_pk_fp8_f32 v162, v100, v101 op_sel:[0,0,1]
	global_load_lds_dwordx4 v[114:115], off
	ds_read_b128 v[210:213], v183 offset:0
	ds_read_b128 v[214:217], v190 offset:0
	ds_read_b128 v[218:221], v183 offset:0x800
	ds_read_b128 v[222:225], v190 offset:0x800
	v_cvt_pk_fp8_f32 v163, v104, v105 op_sel:[0,0,1]
	s_waitcnt lgkmcnt(2)
	v_mfma_f32_32x32x64_f8f6f4 v[114:129], v[210:217], v[154:161], v[82:97]
	v_cvt_pk_fp8_f32 v164, v106, v107
	v_cvt_pk_fp8_f32 v165, v110, v111
	ds_read_b128 v[226:229], v194 offset:0
	ds_read_b128 v[230:233], v195 offset:0
	v_cvt_pk_fp8_f32 v164, v108, v109 op_sel:[0,0,1]
	v_cvt_pk_fp8_f32 v165, v112, v113 op_sel:[0,0,1]
	s_waitcnt lgkmcnt(2)
	v_mfma_f32_32x32x64_f8f6f4 v[98:113], v[218:225], v[154:161], v[82:97]
	v_cvt_pk_fp8_f32 v166, v130, v131
	v_cvt_pk_fp8_f32 v167, v134, v135
	v_cvt_pk_fp8_f32 v168, v138, v139
	v_cvt_pk_fp8_f32 v169, v142, v143
	v_cvt_pk_fp8_f32 v166, v132, v133 op_sel:[0,0,1]
	v_cvt_pk_fp8_f32 v167, v136, v137 op_sel:[0,0,1]
	v_cvt_pk_fp8_f32 v168, v140, v141 op_sel:[0,0,1]
	v_cvt_pk_fp8_f32 v169, v144, v145 op_sel:[0,0,1]
	s_nop 0
	ds_read_b128 v[138:141], v194 offset:0x800
	ds_read_b128 v[142:145], v195 offset:0x800
	s_nop 0
	v_mfma_f32_16x16x128_f8f6f4 v[18:21], v[162:169], v[146:153], v[18:21]
	s_waitcnt lgkmcnt(2)
	v_mfma_f32_32x32x64_f8f6f4 v[2:17], v[162:169], v[226:233], v[2:17]
	ds_read_b128 v[130:133], v194 offset:0x1000
	ds_read_b128 v[134:137], v195 offset:0x1000
